# GEMM K loops: LDS-read wait moved from before the pre-MFMA s_barrier to after it (36 sites), on top of v44
# baseline (speedup 1.0000x reference)
.LBB0_339:
	s_add_u32 s26, s24, 0xfff80080
	s_addc_u32 s27, s25, -1
	s_add_i32 s82, 0, 0x10000
	s_cmp_eq_u32 s81, 28
	s_cselect_b32 s27, s21, s27
	s_cselect_b32 s26, s20, s26
	v_add_u32_e32 v96, s82, v141
	s_cselect_b32 s29, s23, s80
	s_cselect_b32 s28, s22, s79
	s_add_i32 s84, 0, 0x14000
	ds_read_b128 v[144:147], v96
	ds_read_b128 v[148:151], v96 offset:1024
	ds_read_b128 v[152:155], v96 offset:2048
	ds_read_b128 v[156:159], v96 offset:3072
	v_add_u32_e32 v96, s84, v141
	ds_read_b128 v[160:163], v96
	ds_read_b128 v[164:167], v96 offset:1024
	ds_read_b128 v[168:171], v96 offset:2048
	ds_read_b128 v[172:175], v96 offset:3072
	v_mov_b32_e32 v96, v136
	ds_read_b128 v[176:179], v142
	ds_read_b128 v[180:183], v142 offset:1024
	ds_read_b128 v[184:187], v142 offset:2048
	ds_read_b128 v[188:191], v142 offset:3072
	ds_read_b128 v[192:195], v142 offset:4096
	ds_read_b128 v[196:199], v142 offset:5120
	ds_read_b128 v[200:203], v142 offset:6144
	ds_read_b128 v[222:225], v142 offset:7168
	s_add_i32 m0, s36, 0xc000
	s_nop 0
	global_load_lds_dwordx4 v96, s[24:25]
	v_mov_b32_e32 v96, v138
	s_add_i32 m0, s36, 0xe000
	s_nop 0
	global_load_lds_dwordx4 v96, s[24:25]
	s_waitcnt vmcnt(8)
	s_nop 0
	s_barrier
	s_setprio 1
	s_waitcnt lgkmcnt(0)
	v_mfma_f32_16x16x32_bf16 v[126:129], v[144:147], v[176:179], v[126:129]
	v_mfma_f32_16x16x32_bf16 v[122:125], v[152:155], v[176:179], v[122:125]
	v_mfma_f32_16x16x32_bf16 v[118:121], v[144:147], v[184:187], v[118:121]
	v_mfma_f32_16x16x32_bf16 v[114:117], v[152:155], v[184:187], v[114:117]
	v_mfma_f32_16x16x32_bf16 v[102:105], v[144:147], v[192:195], v[102:105]
	v_mfma_f32_16x16x32_bf16 v[98:101], v[152:155], v[192:195], v[98:101]
	v_mfma_f32_16x16x32_bf16 v[84:87], v[144:147], v[200:203], v[84:87]
	v_mfma_f32_16x16x32_bf16 v[80:83], v[152:155], v[200:203], v[80:83]
	v_mfma_f32_16x16x32_bf16 v[126:129], v[148:151], v[180:183], v[126:129]
	v_mfma_f32_16x16x32_bf16 v[122:125], v[156:159], v[180:183], v[122:125]
	v_mfma_f32_16x16x32_bf16 v[118:121], v[148:151], v[188:191], v[118:121]
	v_mfma_f32_16x16x32_bf16 v[114:117], v[156:159], v[188:191], v[114:117]
	v_mfma_f32_16x16x32_bf16 v[102:105], v[148:151], v[196:199], v[102:105]
	v_mfma_f32_16x16x32_bf16 v[98:101], v[156:159], v[196:199], v[98:101]
	v_mfma_f32_16x16x32_bf16 v[84:87], v[148:151], v[222:225], v[84:87]
	v_mfma_f32_16x16x32_bf16 v[80:83], v[156:159], v[222:225], v[80:83]
	s_setprio 0
	s_setprio 1
	v_mfma_f32_16x16x32_bf16 v[110:113], v[160:163], v[176:179], v[110:113]
	v_mfma_f32_16x16x32_bf16 v[106:109], v[168:171], v[176:179], v[106:109]
	v_mfma_f32_16x16x32_bf16 v[92:95], v[160:163], v[184:187], v[92:95]
	v_mfma_f32_16x16x32_bf16 v[88:91], v[168:171], v[184:187], v[88:91]
	v_mfma_f32_16x16x32_bf16 v[76:79], v[160:163], v[192:195], v[76:79]
	v_mfma_f32_16x16x32_bf16 v[72:75], v[168:171], v[192:195], v[72:75]
	v_mfma_f32_16x16x32_bf16 v[68:71], v[160:163], v[200:203], v[68:71]
	v_mfma_f32_16x16x32_bf16 v[64:67], v[168:171], v[200:203], v[64:67]
	v_mfma_f32_16x16x32_bf16 v[110:113], v[164:167], v[180:183], v[110:113]
	v_mfma_f32_16x16x32_bf16 v[106:109], v[172:175], v[180:183], v[106:109]
	v_mfma_f32_16x16x32_bf16 v[92:95], v[164:167], v[188:191], v[92:95]
	v_mfma_f32_16x16x32_bf16 v[88:91], v[172:175], v[188:191], v[88:91]
	v_mfma_f32_16x16x32_bf16 v[76:79], v[164:167], v[196:199], v[76:79]
	v_mfma_f32_16x16x32_bf16 v[72:75], v[172:175], v[196:199], v[72:75]
	v_mfma_f32_16x16x32_bf16 v[68:71], v[164:167], v[222:225], v[68:71]
	v_mfma_f32_16x16x32_bf16 v[64:67], v[172:175], v[222:225], v[64:67]
	s_setprio 0
	s_barrier
	v_mov_b32_e32 v96, v137
	s_add_i32 s82, s82, s35
	ds_read_b128 v[176:179], v142 offset:16384
	ds_read_b128 v[180:183], v142 offset:17408
	ds_read_b128 v[184:187], v142 offset:18432
	ds_read_b128 v[188:191], v142 offset:19456
	ds_read_b128 v[192:195], v142 offset:20480
	ds_read_b128 v[196:199], v142 offset:21504
	ds_read_b128 v[200:203], v142 offset:22528
	ds_read_b128 v[222:225], v142 offset:23552
	s_mov_b32 m0, s82
	s_nop 0
	global_load_lds_dwordx4 v96, s[28:29]
	v_mov_b32_e32 v96, v139
	s_add_i32 m0, s82, 0x2000
	s_add_u32 s82, s28, 0x80000
	global_load_lds_dwordx4 v96, s[28:29]
	s_addc_u32 s83, s29, 0
	v_mov_b32_e32 v96, v137
	s_add_i32 s84, s84, s35
	s_mov_b32 m0, s84
	s_nop 0
	global_load_lds_dwordx4 v96, s[82:83]
	v_mov_b32_e32 v96, v139
	s_add_i32 m0, s84, 0x2000
	s_nop 0
	global_load_lds_dwordx4 v96, s[82:83]
	v_mov_b32_e32 v96, v136
	s_mov_b32 m0, s36
	s_nop 0
	global_load_lds_dwordx4 v96, s[26:27]
	v_mov_b32_e32 v96, v138
	s_mov_b32 m0, s37
	s_nop 0
	global_load_lds_dwordx4 v96, s[26:27]
	s_waitcnt vmcnt(8)
	s_nop 0
	s_barrier
	s_setprio 1
	s_waitcnt lgkmcnt(0)
	v_mfma_f32_16x16x32_bf16 v[60:63], v[144:147], v[176:179], v[60:63]
	v_mfma_f32_16x16x32_bf16 v[56:59], v[152:155], v[176:179], v[56:59]
	v_mfma_f32_16x16x32_bf16 v[52:55], v[144:147], v[184:187], v[52:55]
	v_mfma_f32_16x16x32_bf16 v[48:51], v[152:155], v[184:187], v[48:51]
	v_mfma_f32_16x16x32_bf16 v[36:39], v[144:147], v[192:195], v[36:39]
	v_mfma_f32_16x16x32_bf16 v[32:35], v[152:155], v[192:195], v[32:35]
	v_mfma_f32_16x16x32_bf16 v[20:23], v[144:147], v[200:203], v[20:23]
	v_mfma_f32_16x16x32_bf16 v[16:19], v[152:155], v[200:203], v[16:19]
	v_mfma_f32_16x16x32_bf16 v[60:63], v[148:151], v[180:183], v[60:63]
	v_mfma_f32_16x16x32_bf16 v[56:59], v[156:159], v[180:183], v[56:59]
	v_mfma_f32_16x16x32_bf16 v[52:55], v[148:151], v[188:191], v[52:55]
	v_mfma_f32_16x16x32_bf16 v[48:51], v[156:159], v[188:191], v[48:51]
	v_mfma_f32_16x16x32_bf16 v[36:39], v[148:151], v[196:199], v[36:39]
	v_mfma_f32_16x16x32_bf16 v[32:35], v[156:159], v[196:199], v[32:35]
	v_mfma_f32_16x16x32_bf16 v[20:23], v[148:151], v[222:225], v[20:23]
	v_mfma_f32_16x16x32_bf16 v[16:19], v[156:159], v[222:225], v[16:19]
	s_setprio 0
	s_setprio 1
	v_mfma_f32_16x16x32_bf16 v[44:47], v[160:163], v[176:179], v[44:47]
	v_mfma_f32_16x16x32_bf16 v[40:43], v[168:171], v[176:179], v[40:43]
	v_mfma_f32_16x16x32_bf16 v[28:31], v[160:163], v[184:187], v[28:31]
	v_mfma_f32_16x16x32_bf16 v[24:27], v[168:171], v[184:187], v[24:27]
	v_mfma_f32_16x16x32_bf16 v[12:15], v[160:163], v[192:195], v[12:15]
	v_mfma_f32_16x16x32_bf16 v[8:11], v[168:171], v[192:195], v[8:11]
	v_mfma_f32_16x16x32_bf16 v[4:7], v[160:163], v[200:203], v[4:7]
	v_mfma_f32_16x16x32_bf16 v[0:3], v[168:171], v[200:203], v[0:3]
	v_mfma_f32_16x16x32_bf16 v[44:47], v[164:167], v[180:183], v[44:47]
	v_mfma_f32_16x16x32_bf16 v[40:43], v[172:175], v[180:183], v[40:43]
	v_mfma_f32_16x16x32_bf16 v[28:31], v[164:167], v[188:191], v[28:31]
	v_mfma_f32_16x16x32_bf16 v[24:27], v[172:175], v[188:191], v[24:27]
	v_mfma_f32_16x16x32_bf16 v[12:15], v[164:167], v[196:199], v[12:15]
	v_mfma_f32_16x16x32_bf16 v[8:11], v[172:175], v[196:199], v[8:11]
	v_mfma_f32_16x16x32_bf16 v[4:7], v[164:167], v[222:225], v[4:7]
	v_mfma_f32_16x16x32_bf16 v[0:3], v[172:175], v[222:225], v[0:3]
	s_setprio 0
	s_barrier
	s_add_i32 s84, 0, 0x18000
	v_add_u32_e32 v96, s84, v141
	s_add_i32 s85, 0, 0x1c000
	ds_read_b128 v[144:147], v96
	ds_read_b128 v[148:151], v96 offset:1024
	ds_read_b128 v[152:155], v96 offset:2048
	ds_read_b128 v[156:159], v96 offset:3072
	v_add_u32_e32 v96, s85, v141
	ds_read_b128 v[160:163], v96
	ds_read_b128 v[164:167], v96 offset:1024
	ds_read_b128 v[168:171], v96 offset:2048
	ds_read_b128 v[172:175], v96 offset:3072
	s_add_u32 s82, s26, 0x80000
	v_mov_b32_e32 v96, v136
	s_mov_b32 m0, s38
	ds_read_b128 v[176:179], v142 offset:32768
	ds_read_b128 v[180:183], v142 offset:33792
	ds_read_b128 v[184:187], v142 offset:34816
	ds_read_b128 v[188:191], v142 offset:35840
	ds_read_b128 v[192:195], v142 offset:36864
	ds_read_b128 v[196:199], v142 offset:37888
	ds_read_b128 v[200:203], v142 offset:38912
	ds_read_b128 v[222:225], v142 offset:39936
	s_addc_u32 s83, s27, 0
	s_nop 0
	global_load_lds_dwordx4 v96, s[82:83]
	v_mov_b32_e32 v96, v138
	s_mov_b32 m0, s39
	s_nop 0
	global_load_lds_dwordx4 v96, s[82:83]
	s_waitcnt vmcnt(8)
	s_nop 0
	s_barrier
	s_setprio 1
	s_waitcnt lgkmcnt(0)
	v_mfma_f32_16x16x32_bf16 v[126:129], v[144:147], v[176:179], v[126:129]
	v_mfma_f32_16x16x32_bf16 v[122:125], v[152:155], v[176:179], v[122:125]
	v_mfma_f32_16x16x32_bf16 v[118:121], v[144:147], v[184:187], v[118:121]
	v_mfma_f32_16x16x32_bf16 v[114:117], v[152:155], v[184:187], v[114:117]
	v_mfma_f32_16x16x32_bf16 v[102:105], v[144:147], v[192:195], v[102:105]
	v_mfma_f32_16x16x32_bf16 v[98:101], v[152:155], v[192:195], v[98:101]
	v_mfma_f32_16x16x32_bf16 v[84:87], v[144:147], v[200:203], v[84:87]
	v_mfma_f32_16x16x32_bf16 v[80:83], v[152:155], v[200:203], v[80:83]
	v_mfma_f32_16x16x32_bf16 v[126:129], v[148:151], v[180:183], v[126:129]
	v_mfma_f32_16x16x32_bf16 v[122:125], v[156:159], v[180:183], v[122:125]
	v_mfma_f32_16x16x32_bf16 v[118:121], v[148:151], v[188:191], v[118:121]
	v_mfma_f32_16x16x32_bf16 v[114:117], v[156:159], v[188:191], v[114:117]
	v_mfma_f32_16x16x32_bf16 v[102:105], v[148:151], v[196:199], v[102:105]
	v_mfma_f32_16x16x32_bf16 v[98:101], v[156:159], v[196:199], v[98:101]
	v_mfma_f32_16x16x32_bf16 v[84:87], v[148:151], v[222:225], v[84:87]
	v_mfma_f32_16x16x32_bf16 v[80:83], v[156:159], v[222:225], v[80:83]
	s_setprio 0
	s_setprio 1
	v_mfma_f32_16x16x32_bf16 v[110:113], v[160:163], v[176:179], v[110:113]
	v_mfma_f32_16x16x32_bf16 v[106:109], v[168:171], v[176:179], v[106:109]
	v_mfma_f32_16x16x32_bf16 v[92:95], v[160:163], v[184:187], v[92:95]
	v_mfma_f32_16x16x32_bf16 v[88:91], v[168:171], v[184:187], v[88:91]
	v_mfma_f32_16x16x32_bf16 v[76:79], v[160:163], v[192:195], v[76:79]
	v_mfma_f32_16x16x32_bf16 v[72:75], v[168:171], v[192:195], v[72:75]
	v_mfma_f32_16x16x32_bf16 v[68:71], v[160:163], v[200:203], v[68:71]
	v_mfma_f32_16x16x32_bf16 v[64:67], v[168:171], v[200:203], v[64:67]
	v_mfma_f32_16x16x32_bf16 v[110:113], v[164:167], v[180:183], v[110:113]
	v_mfma_f32_16x16x32_bf16 v[106:109], v[172:175], v[180:183], v[106:109]
	v_mfma_f32_16x16x32_bf16 v[92:95], v[164:167], v[188:191], v[92:95]
	v_mfma_f32_16x16x32_bf16 v[88:91], v[172:175], v[188:191], v[88:91]
	v_mfma_f32_16x16x32_bf16 v[76:79], v[164:167], v[196:199], v[76:79]
	v_mfma_f32_16x16x32_bf16 v[72:75], v[172:175], v[196:199], v[72:75]
	v_mfma_f32_16x16x32_bf16 v[68:71], v[164:167], v[222:225], v[68:71]
	v_mfma_f32_16x16x32_bf16 v[64:67], v[172:175], v[222:225], v[64:67]
	s_setprio 0
	s_barrier
	v_mov_b32_e32 v96, v137
	ds_read_b128 v[176:179], v142 offset:49152
	ds_read_b128 v[180:183], v142 offset:50176
	ds_read_b128 v[184:187], v142 offset:51200
	ds_read_b128 v[188:191], v142 offset:52224
	ds_read_b128 v[192:195], v142 offset:53248
	ds_read_b128 v[196:199], v142 offset:54272
	ds_read_b128 v[200:203], v142 offset:55296
	ds_read_b128 v[222:225], v142 offset:56320
	s_add_i32 s82, s84, s35
	v_lshl_add_u64 v[134:135], s[28:29], 0, v[96:97]
	v_lshl_add_u64 v[134:135], v[134:135], 0, s[0:1]
	s_mov_b32 m0, s82
	v_mov_b32_e32 v96, v139
	global_load_lds_dwordx4 v[134:135], off
	s_add_i32 m0, s82, 0x2000
	s_nop 0
	v_lshl_add_u64 v[134:135], s[28:29], 0, v[96:97]
	s_add_u32 s28, s28, 0x80080
	v_lshl_add_u64 v[134:135], v[134:135], 0, s[0:1]
	s_addc_u32 s29, s29, 0
	v_mov_b32_e32 v96, v137
	s_add_i32 s82, s85, s35
	global_load_lds_dwordx4 v[134:135], off
	s_mov_b32 m0, s82
	s_nop 0
	global_load_lds_dwordx4 v96, s[28:29]
	v_mov_b32_e32 v96, v139
	s_add_i32 m0, s82, 0x2000
	s_nop 0
	global_load_lds_dwordx4 v96, s[28:29]
	v_mov_b32_e32 v96, v136
	s_mov_b32 m0, s40
	v_lshl_add_u64 v[134:135], s[26:27], 0, v[96:97]
	v_lshl_add_u64 v[134:135], v[134:135], 0, s[0:1]
	v_mov_b32_e32 v96, v138
	global_load_lds_dwordx4 v[134:135], off
	s_mov_b32 m0, s41
	v_lshl_add_u64 v[134:135], s[26:27], 0, v[96:97]
	v_lshl_add_u64 v[134:135], v[134:135], 0, s[0:1]
	global_load_lds_dwordx4 v[134:135], off
	s_waitcnt vmcnt(8)
	s_nop 0
	s_barrier
	s_setprio 1
	s_waitcnt lgkmcnt(0)
	v_mfma_f32_16x16x32_bf16 v[60:63], v[144:147], v[176:179], v[60:63]
	v_mfma_f32_16x16x32_bf16 v[56:59], v[152:155], v[176:179], v[56:59]
	v_mfma_f32_16x16x32_bf16 v[52:55], v[144:147], v[184:187], v[52:55]
	v_mfma_f32_16x16x32_bf16 v[48:51], v[152:155], v[184:187], v[48:51]
	v_mfma_f32_16x16x32_bf16 v[36:39], v[144:147], v[192:195], v[36:39]
	v_mfma_f32_16x16x32_bf16 v[32:35], v[152:155], v[192:195], v[32:35]
	v_mfma_f32_16x16x32_bf16 v[20:23], v[144:147], v[200:203], v[20:23]
	v_mfma_f32_16x16x32_bf16 v[16:19], v[152:155], v[200:203], v[16:19]
	v_mfma_f32_16x16x32_bf16 v[60:63], v[148:151], v[180:183], v[60:63]
	v_mfma_f32_16x16x32_bf16 v[56:59], v[156:159], v[180:183], v[56:59]
	v_mfma_f32_16x16x32_bf16 v[52:55], v[148:151], v[188:191], v[52:55]
	v_mfma_f32_16x16x32_bf16 v[48:51], v[156:159], v[188:191], v[48:51]
	v_mfma_f32_16x16x32_bf16 v[36:39], v[148:151], v[196:199], v[36:39]
	v_mfma_f32_16x16x32_bf16 v[32:35], v[156:159], v[196:199], v[32:35]
	v_mfma_f32_16x16x32_bf16 v[20:23], v[148:151], v[222:225], v[20:23]
	v_mfma_f32_16x16x32_bf16 v[16:19], v[156:159], v[222:225], v[16:19]
	s_setprio 0
	s_setprio 1
	v_mfma_f32_16x16x32_bf16 v[44:47], v[160:163], v[176:179], v[44:47]
	v_mfma_f32_16x16x32_bf16 v[40:43], v[168:171], v[176:179], v[40:43]
	v_mfma_f32_16x16x32_bf16 v[28:31], v[160:163], v[184:187], v[28:31]
	v_mfma_f32_16x16x32_bf16 v[24:27], v[168:171], v[184:187], v[24:27]
	v_mfma_f32_16x16x32_bf16 v[12:15], v[160:163], v[192:195], v[12:15]
	v_mfma_f32_16x16x32_bf16 v[8:11], v[168:171], v[192:195], v[8:11]
	v_mfma_f32_16x16x32_bf16 v[4:7], v[160:163], v[200:203], v[4:7]
	v_mfma_f32_16x16x32_bf16 v[0:3], v[168:171], v[200:203], v[0:3]
	v_mfma_f32_16x16x32_bf16 v[44:47], v[164:167], v[180:183], v[44:47]
	v_mfma_f32_16x16x32_bf16 v[40:43], v[172:175], v[180:183], v[40:43]
	v_mfma_f32_16x16x32_bf16 v[28:31], v[164:167], v[188:191], v[28:31]
	v_mfma_f32_16x16x32_bf16 v[24:27], v[172:175], v[188:191], v[24:27]
	v_mfma_f32_16x16x32_bf16 v[12:15], v[164:167], v[196:199], v[12:15]
	v_mfma_f32_16x16x32_bf16 v[8:11], v[172:175], v[196:199], v[8:11]
	v_mfma_f32_16x16x32_bf16 v[4:7], v[164:167], v[222:225], v[4:7]
	v_mfma_f32_16x16x32_bf16 v[0:3], v[172:175], v[222:225], v[0:3]
	s_setprio 0
	s_barrier
	s_add_i32 s81, s81, 2
	s_add_u32 s79, s79, 0x100
	s_addc_u32 s80, s80, 0
	s_add_u32 s24, s24, 0x100
	s_addc_u32 s25, s25, 0
	s_cmp_gt_u32 s81, 29
	s_cbranch_scc0 .LBB0_339
	s_and_b64 vcc, exec, s[10:11]
	s_cbranch_vccz .LBB0_344
	s_barrier
	v_lshl_add_u32 v134, s78, 8, v140
	s_cmp_gt_i32 s47, 53
	s_mov_b64 s[20:21], -1
	s_cbranch_scc1 .LBB0_345

.LBB0_370:
	s_add_u32 s22, s20, 0xfff80080
	s_addc_u32 s23, s21, -1
	s_add_i32 s46, 0, 0x10000
	s_cmp_eq_u32 s45, 12
	s_cselect_b32 s23, s17, s23
	s_cselect_b32 s22, s16, s22
	v_add_u32_e32 v96, s46, v139
	s_cselect_b32 s25, s19, s44
	s_cselect_b32 s24, s18, s43
	s_add_i32 s78, 0, 0x14000
	ds_read_b128 v[142:145], v96
	ds_read_b128 v[146:149], v96 offset:1024
	ds_read_b128 v[150:153], v96 offset:2048
	ds_read_b128 v[154:157], v96 offset:3072
	v_add_u32_e32 v96, s78, v139
	ds_read_b128 v[158:161], v96
	ds_read_b128 v[162:165], v96 offset:1024
	ds_read_b128 v[166:169], v96 offset:2048
	ds_read_b128 v[170:173], v96 offset:3072
	v_mov_b32_e32 v96, v134
	ds_read_b128 v[174:177], v140
	ds_read_b128 v[178:181], v140 offset:1024
	ds_read_b128 v[182:185], v140 offset:2048
	ds_read_b128 v[186:189], v140 offset:3072
	ds_read_b128 v[190:193], v140 offset:4096
	ds_read_b128 v[194:197], v140 offset:5120
	ds_read_b128 v[222:225], v140 offset:6144
	ds_read_b128 v[226:229], v140 offset:7168
	s_add_i32 m0, s28, 0xc000
	s_nop 0
	global_load_lds_dwordx4 v96, s[20:21]
	v_mov_b32_e32 v96, v136
	s_add_i32 m0, s28, 0xe000
	s_nop 0
	global_load_lds_dwordx4 v96, s[20:21]
	s_waitcnt vmcnt(8)
	s_nop 0
	s_barrier
	s_setprio 1
	s_waitcnt lgkmcnt(0)
	v_mfma_f32_16x16x128_f8f6f4 v[126:129], v[142:149], v[174:181], v[126:129]
	v_mfma_f32_16x16x128_f8f6f4 v[122:125], v[150:157], v[174:181], v[122:125]
	v_mfma_f32_16x16x128_f8f6f4 v[110:113], v[142:149], v[182:189], v[110:113]
	v_mfma_f32_16x16x128_f8f6f4 v[106:109], v[150:157], v[182:189], v[106:109]
	v_mfma_f32_16x16x128_f8f6f4 v[198:201], v[142:149], v[190:197], v[92:95]
	v_mfma_f32_16x16x128_f8f6f4 v[230:233], v[150:157], v[190:197], v[88:91]
	v_mfma_f32_16x16x128_f8f6f4 v[234:237], v[142:149], v[222:229], v[76:79]
	v_mfma_f32_16x16x128_f8f6f4 v[238:241], v[150:157], v[222:229], v[72:75]
	s_setprio 0
	s_setprio 1
	v_mfma_f32_16x16x128_f8f6f4 v[118:121], v[158:165], v[174:181], v[118:121]
	v_mfma_f32_16x16x128_f8f6f4 v[114:117], v[166:173], v[174:181], v[114:117]
	v_mfma_f32_16x16x128_f8f6f4 v[102:105], v[158:165], v[182:189], v[102:105]
	v_mfma_f32_16x16x128_f8f6f4 v[98:101], v[166:173], v[182:189], v[98:101]
	v_mfma_f32_16x16x128_f8f6f4 v[174:177], v[158:165], v[190:197], v[84:87]
	v_mfma_f32_16x16x128_f8f6f4 v[178:181], v[166:173], v[190:197], v[80:83]
	v_mfma_f32_16x16x128_f8f6f4 v[182:185], v[158:165], v[222:229], v[68:71]
	v_mfma_f32_16x16x128_f8f6f4 v[186:189], v[166:173], v[222:229], v[64:67]
	s_setprio 0
	s_barrier
	v_mov_b32_e32 v96, v135
	s_add_i32 s46, s46, s27
	s_nop 2
	ds_read_b128 v[64:67], v140 offset:16384
	ds_read_b128 v[68:71], v140 offset:17408
	ds_read_b128 v[72:75], v140 offset:18432
	ds_read_b128 v[76:79], v140 offset:19456
	ds_read_b128 v[80:83], v140 offset:20480
	ds_read_b128 v[84:87], v140 offset:21504
	ds_read_b128 v[88:91], v140 offset:22528
	ds_read_b128 v[92:95], v140 offset:23552
	s_mov_b32 m0, s46
	s_nop 0
	global_load_lds_dwordx4 v96, s[24:25]
	v_mov_b32_e32 v96, v137
	s_add_i32 m0, s46, 0x2000
	s_add_u32 s46, s24, 0x80000
	global_load_lds_dwordx4 v96, s[24:25]
	s_addc_u32 s47, s25, 0
	v_mov_b32_e32 v96, v135
	s_add_i32 s78, s78, s27
	s_mov_b32 m0, s78
	s_nop 0
	global_load_lds_dwordx4 v96, s[46:47]
	v_mov_b32_e32 v96, v137
	s_add_i32 m0, s78, 0x2000
	s_nop 0
	global_load_lds_dwordx4 v96, s[46:47]
	v_mov_b32_e32 v96, v134
	s_mov_b32 m0, s28
	s_nop 0
	global_load_lds_dwordx4 v96, s[22:23]
	v_mov_b32_e32 v96, v136
	s_mov_b32 m0, s29
	s_nop 0
	global_load_lds_dwordx4 v96, s[22:23]
	s_waitcnt vmcnt(8)
	s_nop 0
	s_barrier
	s_setprio 1
	s_waitcnt lgkmcnt(0)
	v_mfma_f32_16x16x128_f8f6f4 v[60:63], v[142:149], v[64:71], v[60:63]
	v_mfma_f32_16x16x128_f8f6f4 v[56:59], v[150:157], v[64:71], v[56:59]
	v_mfma_f32_16x16x128_f8f6f4 v[190:193], v[142:149], v[72:79], v[44:47]
	v_mfma_f32_16x16x128_f8f6f4 v[194:197], v[150:157], v[72:79], v[40:43]
	v_mfma_f32_16x16x128_f8f6f4 v[222:225], v[142:149], v[80:87], v[28:31]
	v_mfma_f32_16x16x128_f8f6f4 v[226:229], v[150:157], v[80:87], v[24:27]
	v_mfma_f32_16x16x128_f8f6f4 v[242:245], v[142:149], v[88:95], v[12:15]
	v_mfma_f32_16x16x128_f8f6f4 v[246:249], v[150:157], v[88:95], v[8:11]
	s_setprio 0
	s_setprio 1
	v_mfma_f32_16x16x128_f8f6f4 v[52:55], v[158:165], v[64:71], v[52:55]
	v_mfma_f32_16x16x128_f8f6f4 v[48:51], v[166:173], v[64:71], v[48:51]
	v_mfma_f32_16x16x128_f8f6f4 v[250:253], v[158:165], v[72:79], v[36:39]
	v_mfma_f32_16x16x128_f8f6f4 v[208:211], v[166:173], v[72:79], v[32:35]
	v_mfma_f32_16x16x128_f8f6f4 v[218:221], v[158:165], v[80:87], v[20:23]
	v_mfma_f32_16x16x128_f8f6f4 v[202:205], v[166:173], v[80:87], v[16:19]
	v_mfma_f32_16x16x128_f8f6f4 v[212:215], v[158:165], v[88:95], v[4:7]
	v_mfma_f32_16x16x128_f8f6f4 v[130:133], v[166:173], v[88:95], v[0:3]
	s_setprio 0
	s_barrier
	s_add_i32 s78, 0, 0x18000
	v_add_u32_e32 v8, s78, v139
	s_add_i32 s79, 0, 0x1c000
	s_nop 1
	ds_read_b128 v[0:3], v8
	ds_read_b128 v[4:7], v8 offset:1024
	ds_read_b128 v[16:19], v8 offset:2048
	ds_read_b128 v[20:23], v8 offset:3072
	v_add_u32_e32 v8, s79, v139
	ds_read_b128 v[142:145], v8
	ds_read_b128 v[146:149], v8 offset:1024
	ds_read_b128 v[150:153], v8 offset:2048
	ds_read_b128 v[154:157], v8 offset:3072
	s_add_u32 s46, s22, 0x80000
	v_mov_b32_e32 v64, v134
	s_mov_b32 m0, s30
	ds_read_b128 v[8:11], v140 offset:32768
	ds_read_b128 v[12:15], v140 offset:33792
	ds_read_b128 v[24:27], v140 offset:34816
	ds_read_b128 v[28:31], v140 offset:35840
	ds_read_b128 v[32:35], v140 offset:36864
	ds_read_b128 v[36:39], v140 offset:37888
	ds_read_b128 v[40:43], v140 offset:38912
	ds_read_b128 v[44:47], v140 offset:39936
	s_addc_u32 s47, s23, 0
	s_nop 0
	global_load_lds_dwordx4 v64, s[46:47]
	v_mov_b32_e32 v64, v136
	s_mov_b32 m0, s31
	s_nop 0
	global_load_lds_dwordx4 v64, s[46:47]
	s_waitcnt vmcnt(8)
	s_nop 0
	s_barrier
	s_setprio 1
	s_waitcnt lgkmcnt(0)
	v_mfma_f32_16x16x128_f8f6f4 v[126:129], v[0:7], v[8:15], v[126:129]
	v_mfma_f32_16x16x128_f8f6f4 v[122:125], v[16:23], v[8:15], v[122:125]
	v_mfma_f32_16x16x128_f8f6f4 v[110:113], v[0:7], v[24:31], v[110:113]
	v_mfma_f32_16x16x128_f8f6f4 v[106:109], v[16:23], v[24:31], v[106:109]
	v_mfma_f32_16x16x128_f8f6f4 v[92:95], v[0:7], v[32:39], v[198:201]
	v_mfma_f32_16x16x128_f8f6f4 v[88:91], v[16:23], v[32:39], v[230:233]
	v_mfma_f32_16x16x128_f8f6f4 v[76:79], v[0:7], v[40:47], v[234:237]
	v_mfma_f32_16x16x128_f8f6f4 v[72:75], v[16:23], v[40:47], v[238:241]
	s_setprio 0
	s_setprio 1
	v_mfma_f32_16x16x128_f8f6f4 v[118:121], v[142:149], v[8:15], v[118:121]
	v_mfma_f32_16x16x128_f8f6f4 v[114:117], v[150:157], v[8:15], v[114:117]
	v_mfma_f32_16x16x128_f8f6f4 v[102:105], v[142:149], v[24:31], v[102:105]
	v_mfma_f32_16x16x128_f8f6f4 v[98:101], v[150:157], v[24:31], v[98:101]
	v_mfma_f32_16x16x128_f8f6f4 v[84:87], v[142:149], v[32:39], v[174:177]
	v_mfma_f32_16x16x128_f8f6f4 v[80:83], v[150:157], v[32:39], v[178:181]
	v_mfma_f32_16x16x128_f8f6f4 v[68:71], v[142:149], v[40:47], v[182:185]
	v_mfma_f32_16x16x128_f8f6f4 v[64:67], v[150:157], v[40:47], v[186:189]
	s_setprio 0
	s_barrier
	v_mov_b32_e32 v96, v135
	ds_read_b128 v[32:35], v140 offset:49152
	ds_read_b128 v[36:39], v140 offset:50176
	ds_read_b128 v[158:161], v140 offset:51200
	ds_read_b128 v[162:165], v140 offset:52224
	ds_read_b128 v[166:169], v140 offset:53248
	ds_read_b128 v[170:173], v140 offset:54272
	ds_read_b128 v[174:177], v140 offset:55296
	ds_read_b128 v[178:181], v140 offset:56320
	s_add_i32 s46, s78, s27
	v_lshl_add_u64 v[8:9], s[24:25], 0, v[96:97]
	v_lshl_add_u64 v[8:9], v[8:9], 0, s[0:1]
	s_mov_b32 m0, s46
	v_mov_b32_e32 v96, v137
	global_load_lds_dwordx4 v[8:9], off
	s_add_i32 m0, s46, 0x2000
	v_lshl_add_u64 v[8:9], s[24:25], 0, v[96:97]
	v_lshl_add_u64 v[8:9], v[8:9], 0, s[0:1]
	s_add_u32 s24, s24, 0x80080
	global_load_lds_dwordx4 v[8:9], off
	s_addc_u32 s25, s25, 0
	v_mov_b32_e32 v8, v135
	s_add_i32 s46, s79, s27
	s_mov_b32 m0, s46
	v_mov_b32_e32 v96, v134
	global_load_lds_dwordx4 v8, s[24:25]
	v_mov_b32_e32 v8, v137
	s_add_i32 m0, s46, 0x2000
	s_nop 0
	global_load_lds_dwordx4 v8, s[24:25]
	s_mov_b32 m0, s34
	v_lshl_add_u64 v[8:9], s[22:23], 0, v[96:97]
	v_lshl_add_u64 v[8:9], v[8:9], 0, s[0:1]
	v_mov_b32_e32 v96, v136
	global_load_lds_dwordx4 v[8:9], off
	s_mov_b32 m0, s35
	v_lshl_add_u64 v[8:9], s[22:23], 0, v[96:97]
	v_lshl_add_u64 v[8:9], v[8:9], 0, s[0:1]
	global_load_lds_dwordx4 v[8:9], off
	s_waitcnt vmcnt(8)
	s_nop 0
	s_barrier
	s_setprio 1
	s_waitcnt lgkmcnt(0)
	v_mfma_f32_16x16x128_f8f6f4 v[60:63], v[0:7], v[32:39], v[60:63]
	v_mfma_f32_16x16x128_f8f6f4 v[56:59], v[16:23], v[32:39], v[56:59]
	v_mfma_f32_16x16x128_f8f6f4 v[44:47], v[0:7], v[158:165], v[190:193]
	v_mfma_f32_16x16x128_f8f6f4 v[40:43], v[16:23], v[158:165], v[194:197]
	v_mfma_f32_16x16x128_f8f6f4 v[28:31], v[0:7], v[166:173], v[222:225]
	v_mfma_f32_16x16x128_f8f6f4 v[24:27], v[16:23], v[166:173], v[226:229]
	v_mfma_f32_16x16x128_f8f6f4 v[12:15], v[0:7], v[174:181], v[242:245]
	v_mfma_f32_16x16x128_f8f6f4 v[8:11], v[16:23], v[174:181], v[246:249]
	s_setprio 0
	s_setprio 1
	v_mfma_f32_16x16x128_f8f6f4 v[52:55], v[142:149], v[32:39], v[52:55]
	v_mfma_f32_16x16x128_f8f6f4 v[48:51], v[150:157], v[32:39], v[48:51]
	v_mfma_f32_16x16x128_f8f6f4 v[36:39], v[142:149], v[158:165], v[250:253]
	v_mfma_f32_16x16x128_f8f6f4 v[32:35], v[150:157], v[158:165], v[208:211]
	v_mfma_f32_16x16x128_f8f6f4 v[20:23], v[142:149], v[166:173], v[218:221]
	v_mfma_f32_16x16x128_f8f6f4 v[16:19], v[150:157], v[166:173], v[202:205]
	v_mfma_f32_16x16x128_f8f6f4 v[4:7], v[142:149], v[174:181], v[212:215]
	v_mfma_f32_16x16x128_f8f6f4 v[0:3], v[150:157], v[174:181], v[130:133]
	s_setprio 0
	s_barrier
	s_add_i32 s45, s45, 2
	s_add_u32 s43, s43, 0x100
	s_addc_u32 s44, s44, 0
	s_add_u32 s20, s20, 0x100
	s_addc_u32 s21, s21, 0
	s_cmp_gt_u32 s45, 13
	s_cbranch_scc0 .LBB0_370
	s_and_b64 vcc, exec, s[8:9]
	s_cbranch_vccz .LBB0_373
	s_barrier

.LBB0_1133:
	s_add_u32 s22, s20, 0xfffc0080
	s_addc_u32 s23, s21, -1
	s_add_i32 s80, 0, 0x10000
	s_cmp_eq_u32 s79, 12
	s_cselect_b32 s23, s3, s23
	s_cselect_b32 s22, s2, s22
	v_add_u32_e32 v96, s80, v224
	s_cselect_b32 s25, s19, s78
	s_cselect_b32 s24, s18, s76
	s_add_i32 s82, 0, 0x14000
	ds_read_b128 v[122:125], v96
	ds_read_b128 v[126:129], v96 offset:1024
	ds_read_b128 v[134:137], v96 offset:2048
	ds_read_b128 v[138:141], v96 offset:3072
	v_add_u32_e32 v96, s82, v224
	ds_read_b128 v[146:149], v96
	ds_read_b128 v[150:153], v96 offset:1024
	ds_read_b128 v[154:157], v96 offset:2048
	ds_read_b128 v[158:161], v96 offset:3072
	v_mov_b32_e32 v96, v202
	ds_read_b128 v[162:165], v226
	ds_read_b128 v[166:169], v226 offset:1024
	ds_read_b128 v[170:173], v226 offset:2048
	ds_read_b128 v[174:177], v226 offset:3072
	ds_read_b128 v[178:181], v226 offset:4096
	ds_read_b128 v[182:185], v226 offset:5120
	ds_read_b128 v[186:189], v226 offset:6144
	ds_read_b128 v[190:193], v226 offset:7168
	s_add_i32 m0, s28, 0xc000
	s_nop 0
	global_load_lds_dwordx4 v96, s[20:21]
	v_mov_b32_e32 v96, v221
	s_add_i32 m0, s28, 0xe000
	s_nop 0
	global_load_lds_dwordx4 v96, s[20:21]
	s_waitcnt vmcnt(8)
	s_nop 0
	s_barrier
	s_setprio 1
	s_waitcnt lgkmcnt(0)
	v_mfma_f32_16x16x32_bf16 v[142:145], v[122:125], v[162:165], v[142:145]
	v_mfma_f32_16x16x32_bf16 v[130:133], v[134:137], v[162:165], v[130:133]
	v_mfma_f32_16x16x32_bf16 v[110:113], v[122:125], v[170:173], v[110:113]
	v_mfma_f32_16x16x32_bf16 v[106:109], v[134:137], v[170:173], v[106:109]
	v_mfma_f32_16x16x32_bf16 v[92:95], v[122:125], v[178:181], v[92:95]
	v_mfma_f32_16x16x32_bf16 v[88:91], v[134:137], v[178:181], v[88:91]
	v_mfma_f32_16x16x32_bf16 v[76:79], v[122:125], v[186:189], v[76:79]
	v_mfma_f32_16x16x32_bf16 v[72:75], v[134:137], v[186:189], v[72:75]
	v_mfma_f32_16x16x32_bf16 v[142:145], v[126:129], v[166:169], v[142:145]
	v_mfma_f32_16x16x32_bf16 v[130:133], v[138:141], v[166:169], v[130:133]
	v_mfma_f32_16x16x32_bf16 v[110:113], v[126:129], v[174:177], v[110:113]
	v_mfma_f32_16x16x32_bf16 v[106:109], v[138:141], v[174:177], v[106:109]
	v_mfma_f32_16x16x32_bf16 v[92:95], v[126:129], v[182:185], v[92:95]
	v_mfma_f32_16x16x32_bf16 v[88:91], v[138:141], v[182:185], v[88:91]
	v_mfma_f32_16x16x32_bf16 v[76:79], v[126:129], v[190:193], v[76:79]
	v_mfma_f32_16x16x32_bf16 v[72:75], v[138:141], v[190:193], v[72:75]
	s_setprio 0
	s_setprio 1
	v_mfma_f32_16x16x32_bf16 v[118:121], v[146:149], v[162:165], v[118:121]
	v_mfma_f32_16x16x32_bf16 v[114:117], v[154:157], v[162:165], v[114:117]
	v_mfma_f32_16x16x32_bf16 v[102:105], v[146:149], v[170:173], v[102:105]
	v_mfma_f32_16x16x32_bf16 v[98:101], v[154:157], v[170:173], v[98:101]
	v_mfma_f32_16x16x32_bf16 v[84:87], v[146:149], v[178:181], v[84:87]
	v_mfma_f32_16x16x32_bf16 v[80:83], v[154:157], v[178:181], v[80:83]
	v_mfma_f32_16x16x32_bf16 v[68:71], v[146:149], v[186:189], v[68:71]
	v_mfma_f32_16x16x32_bf16 v[64:67], v[154:157], v[186:189], v[64:67]
	v_mfma_f32_16x16x32_bf16 v[118:121], v[150:153], v[166:169], v[118:121]
	v_mfma_f32_16x16x32_bf16 v[114:117], v[158:161], v[166:169], v[114:117]
	v_mfma_f32_16x16x32_bf16 v[102:105], v[150:153], v[174:177], v[102:105]
	v_mfma_f32_16x16x32_bf16 v[98:101], v[158:161], v[174:177], v[98:101]
	v_mfma_f32_16x16x32_bf16 v[84:87], v[150:153], v[182:185], v[84:87]
	v_mfma_f32_16x16x32_bf16 v[80:83], v[158:161], v[182:185], v[80:83]
	v_mfma_f32_16x16x32_bf16 v[68:71], v[150:153], v[190:193], v[68:71]
	v_mfma_f32_16x16x32_bf16 v[64:67], v[158:161], v[190:193], v[64:67]
	s_setprio 0
	s_barrier
	v_mov_b32_e32 v96, v203
	s_add_i32 s80, s80, s27
	ds_read_b128 v[162:165], v226 offset:16384
	ds_read_b128 v[166:169], v226 offset:17408
	ds_read_b128 v[170:173], v226 offset:18432
	ds_read_b128 v[174:177], v226 offset:19456
	ds_read_b128 v[178:181], v226 offset:20480
	ds_read_b128 v[182:185], v226 offset:21504
	ds_read_b128 v[186:189], v226 offset:22528
	ds_read_b128 v[190:193], v226 offset:23552
	s_mov_b32 m0, s80
	s_nop 0
	global_load_lds_dwordx4 v96, s[24:25]
	v_mov_b32_e32 v96, v222
	s_add_i32 m0, s80, 0x2000
	s_add_u32 s80, s24, 0x40000
	global_load_lds_dwordx4 v96, s[24:25]
	s_addc_u32 s81, s25, 0
	v_mov_b32_e32 v96, v203
	s_add_i32 s82, s82, s27
	s_mov_b32 m0, s82
	s_nop 0
	global_load_lds_dwordx4 v96, s[80:81]
	v_mov_b32_e32 v96, v222
	s_add_i32 m0, s82, 0x2000
	s_nop 0
	global_load_lds_dwordx4 v96, s[80:81]
	v_mov_b32_e32 v96, v202
	s_mov_b32 m0, s28
	s_nop 0
	global_load_lds_dwordx4 v96, s[22:23]
	v_mov_b32_e32 v96, v221
	s_mov_b32 m0, s29
	s_nop 0
	global_load_lds_dwordx4 v96, s[22:23]
	s_waitcnt vmcnt(8)
	s_nop 0
	s_barrier
	s_setprio 1
	s_waitcnt lgkmcnt(0)
	v_mfma_f32_16x16x32_bf16 v[60:63], v[122:125], v[162:165], v[60:63]
	v_mfma_f32_16x16x32_bf16 v[56:59], v[134:137], v[162:165], v[56:59]
	v_mfma_f32_16x16x32_bf16 v[44:47], v[122:125], v[170:173], v[44:47]
	v_mfma_f32_16x16x32_bf16 v[40:43], v[134:137], v[170:173], v[40:43]
	v_mfma_f32_16x16x32_bf16 v[28:31], v[122:125], v[178:181], v[28:31]
	v_mfma_f32_16x16x32_bf16 v[24:27], v[134:137], v[178:181], v[24:27]
	v_mfma_f32_16x16x32_bf16 v[12:15], v[122:125], v[186:189], v[12:15]
	v_mfma_f32_16x16x32_bf16 v[8:11], v[134:137], v[186:189], v[8:11]
	v_mfma_f32_16x16x32_bf16 v[60:63], v[126:129], v[166:169], v[60:63]
	v_mfma_f32_16x16x32_bf16 v[56:59], v[138:141], v[166:169], v[56:59]
	v_mfma_f32_16x16x32_bf16 v[44:47], v[126:129], v[174:177], v[44:47]
	v_mfma_f32_16x16x32_bf16 v[40:43], v[138:141], v[174:177], v[40:43]
	v_mfma_f32_16x16x32_bf16 v[28:31], v[126:129], v[182:185], v[28:31]
	v_mfma_f32_16x16x32_bf16 v[24:27], v[138:141], v[182:185], v[24:27]
	v_mfma_f32_16x16x32_bf16 v[12:15], v[126:129], v[190:193], v[12:15]
	v_mfma_f32_16x16x32_bf16 v[8:11], v[138:141], v[190:193], v[8:11]
	s_setprio 0
	s_setprio 1
	v_mfma_f32_16x16x32_bf16 v[52:55], v[146:149], v[162:165], v[52:55]
	v_mfma_f32_16x16x32_bf16 v[48:51], v[154:157], v[162:165], v[48:51]
	v_mfma_f32_16x16x32_bf16 v[36:39], v[146:149], v[170:173], v[36:39]
	v_mfma_f32_16x16x32_bf16 v[32:35], v[154:157], v[170:173], v[32:35]
	v_mfma_f32_16x16x32_bf16 v[20:23], v[146:149], v[178:181], v[20:23]
	v_mfma_f32_16x16x32_bf16 v[16:19], v[154:157], v[178:181], v[16:19]
	v_mfma_f32_16x16x32_bf16 v[4:7], v[146:149], v[186:189], v[4:7]
	v_mfma_f32_16x16x32_bf16 v[0:3], v[154:157], v[186:189], v[0:3]
	v_mfma_f32_16x16x32_bf16 v[52:55], v[150:153], v[166:169], v[52:55]
	v_mfma_f32_16x16x32_bf16 v[48:51], v[158:161], v[166:169], v[48:51]
	v_mfma_f32_16x16x32_bf16 v[36:39], v[150:153], v[174:177], v[36:39]
	v_mfma_f32_16x16x32_bf16 v[32:35], v[158:161], v[174:177], v[32:35]
	v_mfma_f32_16x16x32_bf16 v[20:23], v[150:153], v[182:185], v[20:23]
	v_mfma_f32_16x16x32_bf16 v[16:19], v[158:161], v[182:185], v[16:19]
	v_mfma_f32_16x16x32_bf16 v[4:7], v[150:153], v[190:193], v[4:7]
	v_mfma_f32_16x16x32_bf16 v[0:3], v[158:161], v[190:193], v[0:3]
	s_setprio 0
	s_barrier
	s_add_i32 s82, 0, 0x18000
	v_add_u32_e32 v96, s82, v224
	s_add_i32 s83, 0, 0x1c000
	ds_read_b128 v[122:125], v96
	ds_read_b128 v[126:129], v96 offset:1024
	ds_read_b128 v[134:137], v96 offset:2048
	ds_read_b128 v[138:141], v96 offset:3072
	v_add_u32_e32 v96, s83, v224
	ds_read_b128 v[146:149], v96
	ds_read_b128 v[150:153], v96 offset:1024
	ds_read_b128 v[154:157], v96 offset:2048
	ds_read_b128 v[158:161], v96 offset:3072
	s_add_u32 s80, s22, 0x40000
	v_mov_b32_e32 v96, v202
	s_mov_b32 m0, s31
	ds_read_b128 v[162:165], v226 offset:32768
	ds_read_b128 v[166:169], v226 offset:33792
	ds_read_b128 v[170:173], v226 offset:34816
	ds_read_b128 v[174:177], v226 offset:35840
	ds_read_b128 v[178:181], v226 offset:36864
	ds_read_b128 v[182:185], v226 offset:37888
	ds_read_b128 v[186:189], v226 offset:38912
	ds_read_b128 v[190:193], v226 offset:39936
	s_addc_u32 s81, s23, 0
	s_nop 0
	global_load_lds_dwordx4 v96, s[80:81]
	v_mov_b32_e32 v96, v221
	s_mov_b32 m0, s34
	s_nop 0
	global_load_lds_dwordx4 v96, s[80:81]
	s_waitcnt vmcnt(8)
	s_nop 0
	s_barrier
	s_setprio 1
	s_waitcnt lgkmcnt(0)
	v_mfma_f32_16x16x32_bf16 v[142:145], v[122:125], v[162:165], v[142:145]
	v_mfma_f32_16x16x32_bf16 v[130:133], v[134:137], v[162:165], v[130:133]
	v_mfma_f32_16x16x32_bf16 v[110:113], v[122:125], v[170:173], v[110:113]
	v_mfma_f32_16x16x32_bf16 v[106:109], v[134:137], v[170:173], v[106:109]
	v_mfma_f32_16x16x32_bf16 v[92:95], v[122:125], v[178:181], v[92:95]
	v_mfma_f32_16x16x32_bf16 v[88:91], v[134:137], v[178:181], v[88:91]
	v_mfma_f32_16x16x32_bf16 v[76:79], v[122:125], v[186:189], v[76:79]
	v_mfma_f32_16x16x32_bf16 v[72:75], v[134:137], v[186:189], v[72:75]
	v_mfma_f32_16x16x32_bf16 v[142:145], v[126:129], v[166:169], v[142:145]
	v_mfma_f32_16x16x32_bf16 v[130:133], v[138:141], v[166:169], v[130:133]
	v_mfma_f32_16x16x32_bf16 v[110:113], v[126:129], v[174:177], v[110:113]
	v_mfma_f32_16x16x32_bf16 v[106:109], v[138:141], v[174:177], v[106:109]
	v_mfma_f32_16x16x32_bf16 v[92:95], v[126:129], v[182:185], v[92:95]
	v_mfma_f32_16x16x32_bf16 v[88:91], v[138:141], v[182:185], v[88:91]
	v_mfma_f32_16x16x32_bf16 v[76:79], v[126:129], v[190:193], v[76:79]
	v_mfma_f32_16x16x32_bf16 v[72:75], v[138:141], v[190:193], v[72:75]
	s_setprio 0
	s_setprio 1
	v_mfma_f32_16x16x32_bf16 v[118:121], v[146:149], v[162:165], v[118:121]
	v_mfma_f32_16x16x32_bf16 v[114:117], v[154:157], v[162:165], v[114:117]
	v_mfma_f32_16x16x32_bf16 v[102:105], v[146:149], v[170:173], v[102:105]
	v_mfma_f32_16x16x32_bf16 v[98:101], v[154:157], v[170:173], v[98:101]
	v_mfma_f32_16x16x32_bf16 v[84:87], v[146:149], v[178:181], v[84:87]
	v_mfma_f32_16x16x32_bf16 v[80:83], v[154:157], v[178:181], v[80:83]
	v_mfma_f32_16x16x32_bf16 v[68:71], v[146:149], v[186:189], v[68:71]
	v_mfma_f32_16x16x32_bf16 v[64:67], v[154:157], v[186:189], v[64:67]
	v_mfma_f32_16x16x32_bf16 v[118:121], v[150:153], v[166:169], v[118:121]
	v_mfma_f32_16x16x32_bf16 v[114:117], v[158:161], v[166:169], v[114:117]
	v_mfma_f32_16x16x32_bf16 v[102:105], v[150:153], v[174:177], v[102:105]
	v_mfma_f32_16x16x32_bf16 v[98:101], v[158:161], v[174:177], v[98:101]
	v_mfma_f32_16x16x32_bf16 v[84:87], v[150:153], v[182:185], v[84:87]
	v_mfma_f32_16x16x32_bf16 v[80:83], v[158:161], v[182:185], v[80:83]
	v_mfma_f32_16x16x32_bf16 v[68:71], v[150:153], v[190:193], v[68:71]
	v_mfma_f32_16x16x32_bf16 v[64:67], v[158:161], v[190:193], v[64:67]
	s_setprio 0
	s_barrier
	v_mov_b32_e32 v96, v203
	ds_read_b128 v[162:165], v226 offset:49152
	ds_read_b128 v[166:169], v226 offset:50176
	ds_read_b128 v[170:173], v226 offset:51200
	ds_read_b128 v[174:177], v226 offset:52224
	ds_read_b128 v[178:181], v226 offset:53248
	ds_read_b128 v[182:185], v226 offset:54272
	ds_read_b128 v[186:189], v226 offset:55296
	ds_read_b128 v[190:193], v226 offset:56320
	s_add_i32 s80, s82, s27
	v_lshl_add_u64 v[194:195], s[24:25], 0, v[96:97]
	v_lshl_add_u64 v[194:195], v[194:195], 0, s[0:1]
	s_mov_b32 m0, s80
	v_mov_b32_e32 v96, v222
	global_load_lds_dwordx4 v[194:195], off
	s_add_i32 m0, s80, 0x2000
	s_nop 0
	v_lshl_add_u64 v[194:195], s[24:25], 0, v[96:97]
	s_add_u32 s24, s24, 0x40080
	v_lshl_add_u64 v[194:195], v[194:195], 0, s[0:1]
	s_addc_u32 s25, s25, 0
	v_mov_b32_e32 v96, v203
	s_add_i32 s80, s83, s27
	global_load_lds_dwordx4 v[194:195], off
	s_mov_b32 m0, s80
	s_nop 0
	global_load_lds_dwordx4 v96, s[24:25]
	v_mov_b32_e32 v96, v222
	s_add_i32 m0, s80, 0x2000
	s_nop 0
	global_load_lds_dwordx4 v96, s[24:25]
	v_mov_b32_e32 v96, v202
	s_mov_b32 m0, s35
	v_lshl_add_u64 v[194:195], s[22:23], 0, v[96:97]
	v_lshl_add_u64 v[194:195], v[194:195], 0, s[0:1]
	v_mov_b32_e32 v96, v221
	global_load_lds_dwordx4 v[194:195], off
	s_mov_b32 m0, s36
	v_lshl_add_u64 v[194:195], s[22:23], 0, v[96:97]
	v_lshl_add_u64 v[194:195], v[194:195], 0, s[0:1]
	global_load_lds_dwordx4 v[194:195], off
	s_waitcnt vmcnt(8)
	s_nop 0
	s_barrier
	s_setprio 1
	s_waitcnt lgkmcnt(0)
	v_mfma_f32_16x16x32_bf16 v[60:63], v[122:125], v[162:165], v[60:63]
	v_mfma_f32_16x16x32_bf16 v[56:59], v[134:137], v[162:165], v[56:59]
	v_mfma_f32_16x16x32_bf16 v[44:47], v[122:125], v[170:173], v[44:47]
	v_mfma_f32_16x16x32_bf16 v[40:43], v[134:137], v[170:173], v[40:43]
	v_mfma_f32_16x16x32_bf16 v[28:31], v[122:125], v[178:181], v[28:31]
	v_mfma_f32_16x16x32_bf16 v[24:27], v[134:137], v[178:181], v[24:27]
	v_mfma_f32_16x16x32_bf16 v[12:15], v[122:125], v[186:189], v[12:15]
	v_mfma_f32_16x16x32_bf16 v[8:11], v[134:137], v[186:189], v[8:11]
	v_mfma_f32_16x16x32_bf16 v[60:63], v[126:129], v[166:169], v[60:63]
	v_mfma_f32_16x16x32_bf16 v[56:59], v[138:141], v[166:169], v[56:59]
	v_mfma_f32_16x16x32_bf16 v[44:47], v[126:129], v[174:177], v[44:47]
	v_mfma_f32_16x16x32_bf16 v[40:43], v[138:141], v[174:177], v[40:43]
	v_mfma_f32_16x16x32_bf16 v[28:31], v[126:129], v[182:185], v[28:31]
	v_mfma_f32_16x16x32_bf16 v[24:27], v[138:141], v[182:185], v[24:27]
	v_mfma_f32_16x16x32_bf16 v[12:15], v[126:129], v[190:193], v[12:15]
	v_mfma_f32_16x16x32_bf16 v[8:11], v[138:141], v[190:193], v[8:11]
	s_setprio 0
	s_setprio 1
	v_mfma_f32_16x16x32_bf16 v[52:55], v[146:149], v[162:165], v[52:55]
	v_mfma_f32_16x16x32_bf16 v[48:51], v[154:157], v[162:165], v[48:51]
	v_mfma_f32_16x16x32_bf16 v[36:39], v[146:149], v[170:173], v[36:39]
	v_mfma_f32_16x16x32_bf16 v[32:35], v[154:157], v[170:173], v[32:35]
	v_mfma_f32_16x16x32_bf16 v[20:23], v[146:149], v[178:181], v[20:23]
	v_mfma_f32_16x16x32_bf16 v[16:19], v[154:157], v[178:181], v[16:19]
	v_mfma_f32_16x16x32_bf16 v[4:7], v[146:149], v[186:189], v[4:7]
	v_mfma_f32_16x16x32_bf16 v[0:3], v[154:157], v[186:189], v[0:3]
	v_mfma_f32_16x16x32_bf16 v[52:55], v[150:153], v[166:169], v[52:55]
	v_mfma_f32_16x16x32_bf16 v[48:51], v[158:161], v[166:169], v[48:51]
	v_mfma_f32_16x16x32_bf16 v[36:39], v[150:153], v[174:177], v[36:39]
	v_mfma_f32_16x16x32_bf16 v[32:35], v[158:161], v[174:177], v[32:35]
	v_mfma_f32_16x16x32_bf16 v[20:23], v[150:153], v[182:185], v[20:23]
	v_mfma_f32_16x16x32_bf16 v[16:19], v[158:161], v[182:185], v[16:19]
	v_mfma_f32_16x16x32_bf16 v[4:7], v[150:153], v[190:193], v[4:7]
	v_mfma_f32_16x16x32_bf16 v[0:3], v[158:161], v[190:193], v[0:3]
	s_setprio 0
	s_barrier
	s_add_i32 s79, s79, 2
	s_add_u32 s76, s76, 0x100
	s_addc_u32 s78, s78, 0
	s_add_u32 s20, s20, 0x100
	s_addc_u32 s21, s21, 0
	s_cmp_gt_u32 s79, 13
	s_cbranch_scc0 .LBB0_1133
	s_and_b64 vcc, exec, s[12:13]
	s_cbranch_vccz .LBB0_1136
	s_barrier

.LBB0_1370:
	s_add_u32 s26, s24, 0xfff80080
	s_addc_u32 s27, s25, -1
	s_add_i32 s82, 0, 0x10000
	s_cmp_eq_u32 s81, 28
	s_cselect_b32 s27, s21, s27
	s_cselect_b32 s26, s20, s26
	v_add_u32_e32 v96, s82, v155
	s_cselect_b32 s29, s23, s80
	s_cselect_b32 s28, s22, s79
	s_add_i32 s84, 0, 0x14000
	ds_read_b128 v[130:133], v96
	ds_read_b128 v[134:137], v96 offset:1024
	ds_read_b128 v[138:141], v96 offset:2048
	ds_read_b128 v[142:145], v96 offset:3072
	v_add_u32_e32 v96, s84, v155
	ds_read_b128 v[146:149], v96
	ds_read_b128 v[158:161], v96 offset:1024
	ds_read_b128 v[162:165], v96 offset:2048
	ds_read_b128 v[166:169], v96 offset:3072
	v_mov_b32_e32 v96, v152
	ds_read_b128 v[170:173], v157
	ds_read_b128 v[174:177], v157 offset:1024
	ds_read_b128 v[178:181], v157 offset:2048
	ds_read_b128 v[182:185], v157 offset:3072
	ds_read_b128 v[186:189], v157 offset:4096
	ds_read_b128 v[190:193], v157 offset:5120
	ds_read_b128 v[194:197], v157 offset:6144
	ds_read_b128 v[198:201], v157 offset:7168
	s_add_i32 m0, s35, 0xc000
	s_nop 0
	global_load_lds_dwordx4 v96, s[24:25]
	v_mov_b32_e32 v96, v153
	s_add_i32 m0, s35, 0xe000
	s_nop 0
	global_load_lds_dwordx4 v96, s[24:25]
	s_waitcnt vmcnt(8)
	s_nop 0
	s_barrier
	s_setprio 1
	s_waitcnt lgkmcnt(0)
	v_mfma_f32_16x16x32_bf16 v[126:129], v[130:133], v[170:173], v[126:129]
	v_mfma_f32_16x16x32_bf16 v[122:125], v[138:141], v[170:173], v[122:125]
	v_mfma_f32_16x16x32_bf16 v[114:117], v[130:133], v[178:181], v[114:117]
	v_mfma_f32_16x16x32_bf16 v[110:113], v[138:141], v[178:181], v[110:113]
	v_mfma_f32_16x16x32_bf16 v[98:101], v[130:133], v[186:189], v[98:101]
	v_mfma_f32_16x16x32_bf16 v[92:95], v[138:141], v[186:189], v[92:95]
	v_mfma_f32_16x16x32_bf16 v[80:83], v[130:133], v[194:197], v[80:83]
	v_mfma_f32_16x16x32_bf16 v[76:79], v[138:141], v[194:197], v[76:79]
	v_mfma_f32_16x16x32_bf16 v[126:129], v[134:137], v[174:177], v[126:129]
	v_mfma_f32_16x16x32_bf16 v[122:125], v[142:145], v[174:177], v[122:125]
	v_mfma_f32_16x16x32_bf16 v[114:117], v[134:137], v[182:185], v[114:117]
	v_mfma_f32_16x16x32_bf16 v[110:113], v[142:145], v[182:185], v[110:113]
	v_mfma_f32_16x16x32_bf16 v[98:101], v[134:137], v[190:193], v[98:101]
	v_mfma_f32_16x16x32_bf16 v[92:95], v[142:145], v[190:193], v[92:95]
	v_mfma_f32_16x16x32_bf16 v[80:83], v[134:137], v[198:201], v[80:83]
	v_mfma_f32_16x16x32_bf16 v[76:79], v[142:145], v[198:201], v[76:79]
	s_setprio 0
	s_setprio 1
	v_mfma_f32_16x16x32_bf16 v[118:121], v[146:149], v[170:173], v[118:121]
	v_mfma_f32_16x16x32_bf16 v[106:109], v[162:165], v[170:173], v[106:109]
	v_mfma_f32_16x16x32_bf16 v[102:105], v[146:149], v[178:181], v[102:105]
	v_mfma_f32_16x16x32_bf16 v[88:91], v[162:165], v[178:181], v[88:91]
	v_mfma_f32_16x16x32_bf16 v[84:87], v[146:149], v[186:189], v[84:87]
	v_mfma_f32_16x16x32_bf16 v[72:75], v[162:165], v[186:189], v[72:75]
	v_mfma_f32_16x16x32_bf16 v[68:71], v[146:149], v[194:197], v[68:71]
	v_mfma_f32_16x16x32_bf16 v[60:63], v[162:165], v[194:197], v[60:63]
	v_mfma_f32_16x16x32_bf16 v[118:121], v[158:161], v[174:177], v[118:121]
	v_mfma_f32_16x16x32_bf16 v[106:109], v[166:169], v[174:177], v[106:109]
	v_mfma_f32_16x16x32_bf16 v[102:105], v[158:161], v[182:185], v[102:105]
	v_mfma_f32_16x16x32_bf16 v[88:91], v[166:169], v[182:185], v[88:91]
	v_mfma_f32_16x16x32_bf16 v[84:87], v[158:161], v[190:193], v[84:87]
	v_mfma_f32_16x16x32_bf16 v[72:75], v[166:169], v[190:193], v[72:75]
	v_mfma_f32_16x16x32_bf16 v[68:71], v[158:161], v[198:201], v[68:71]
	v_mfma_f32_16x16x32_bf16 v[60:63], v[166:169], v[198:201], v[60:63]
	s_setprio 0
	s_barrier
	v_mov_b32_e32 v96, v152
	s_add_i32 s82, s82, s34
	ds_read_b128 v[170:173], v157 offset:16384
	ds_read_b128 v[174:177], v157 offset:17408
	ds_read_b128 v[178:181], v157 offset:18432
	ds_read_b128 v[182:185], v157 offset:19456
	ds_read_b128 v[186:189], v157 offset:20480
	ds_read_b128 v[190:193], v157 offset:21504
	ds_read_b128 v[194:197], v157 offset:22528
	ds_read_b128 v[198:201], v157 offset:23552
	s_mov_b32 m0, s82
	s_nop 0
	global_load_lds_dwordx4 v96, s[28:29]
	v_mov_b32_e32 v96, v153
	s_add_i32 m0, s82, 0x2000
	s_add_u32 s82, s28, 0x80000
	global_load_lds_dwordx4 v96, s[28:29]
	s_addc_u32 s83, s29, 0
	v_mov_b32_e32 v96, v152
	s_add_i32 s84, s84, s34
	s_mov_b32 m0, s84
	s_nop 0
	global_load_lds_dwordx4 v96, s[82:83]
	v_mov_b32_e32 v96, v153
	s_add_i32 m0, s84, 0x2000
	s_nop 0
	global_load_lds_dwordx4 v96, s[82:83]
	v_mov_b32_e32 v96, v152
	s_mov_b32 m0, s35
	s_nop 0
	global_load_lds_dwordx4 v96, s[26:27]
	v_mov_b32_e32 v96, v153
	s_mov_b32 m0, s36
	s_nop 0
	global_load_lds_dwordx4 v96, s[26:27]
	s_waitcnt vmcnt(8)
	s_nop 0
	s_barrier
	s_setprio 1
	s_waitcnt lgkmcnt(0)
	v_mfma_f32_16x16x32_bf16 v[64:67], v[130:133], v[170:173], v[64:67]
	v_mfma_f32_16x16x32_bf16 v[56:59], v[138:141], v[170:173], v[56:59]
	v_mfma_f32_16x16x32_bf16 v[48:51], v[130:133], v[178:181], v[48:51]
	v_mfma_f32_16x16x32_bf16 v[44:47], v[138:141], v[178:181], v[44:47]
	v_mfma_f32_16x16x32_bf16 v[32:35], v[130:133], v[186:189], v[32:35]
	v_mfma_f32_16x16x32_bf16 v[28:31], v[138:141], v[186:189], v[28:31]
	v_mfma_f32_16x16x32_bf16 v[16:19], v[130:133], v[194:197], v[16:19]
	v_mfma_f32_16x16x32_bf16 v[12:15], v[138:141], v[194:197], v[12:15]
	v_mfma_f32_16x16x32_bf16 v[64:67], v[134:137], v[174:177], v[64:67]
	v_mfma_f32_16x16x32_bf16 v[56:59], v[142:145], v[174:177], v[56:59]
	v_mfma_f32_16x16x32_bf16 v[48:51], v[134:137], v[182:185], v[48:51]
	v_mfma_f32_16x16x32_bf16 v[44:47], v[142:145], v[182:185], v[44:47]
	v_mfma_f32_16x16x32_bf16 v[32:35], v[134:137], v[190:193], v[32:35]
	v_mfma_f32_16x16x32_bf16 v[28:31], v[142:145], v[190:193], v[28:31]
	v_mfma_f32_16x16x32_bf16 v[16:19], v[134:137], v[198:201], v[16:19]
	v_mfma_f32_16x16x32_bf16 v[12:15], v[142:145], v[198:201], v[12:15]
	s_setprio 0
	s_setprio 1
	v_mfma_f32_16x16x32_bf16 v[52:55], v[146:149], v[170:173], v[52:55]
	v_mfma_f32_16x16x32_bf16 v[40:43], v[162:165], v[170:173], v[40:43]
	v_mfma_f32_16x16x32_bf16 v[36:39], v[146:149], v[178:181], v[36:39]
	v_mfma_f32_16x16x32_bf16 v[24:27], v[162:165], v[178:181], v[24:27]
	v_mfma_f32_16x16x32_bf16 v[20:23], v[146:149], v[186:189], v[20:23]
	v_mfma_f32_16x16x32_bf16 v[8:11], v[162:165], v[186:189], v[8:11]
	v_mfma_f32_16x16x32_bf16 v[4:7], v[146:149], v[194:197], v[4:7]
	v_mfma_f32_16x16x32_bf16 v[0:3], v[162:165], v[194:197], v[0:3]
	v_mfma_f32_16x16x32_bf16 v[52:55], v[158:161], v[174:177], v[52:55]
	v_mfma_f32_16x16x32_bf16 v[40:43], v[166:169], v[174:177], v[40:43]
	v_mfma_f32_16x16x32_bf16 v[36:39], v[158:161], v[182:185], v[36:39]
	v_mfma_f32_16x16x32_bf16 v[24:27], v[166:169], v[182:185], v[24:27]
	v_mfma_f32_16x16x32_bf16 v[20:23], v[158:161], v[190:193], v[20:23]
	v_mfma_f32_16x16x32_bf16 v[8:11], v[166:169], v[190:193], v[8:11]
	v_mfma_f32_16x16x32_bf16 v[4:7], v[158:161], v[198:201], v[4:7]
	v_mfma_f32_16x16x32_bf16 v[0:3], v[166:169], v[198:201], v[0:3]
	s_setprio 0
	s_barrier
	s_add_i32 s84, 0, 0x18000
	v_add_u32_e32 v96, s84, v155
	s_add_i32 s85, 0, 0x1c000
	ds_read_b128 v[130:133], v96
	ds_read_b128 v[134:137], v96 offset:1024
	ds_read_b128 v[138:141], v96 offset:2048
	ds_read_b128 v[142:145], v96 offset:3072
	v_add_u32_e32 v96, s85, v155
	ds_read_b128 v[146:149], v96
	ds_read_b128 v[158:161], v96 offset:1024
	ds_read_b128 v[162:165], v96 offset:2048
	ds_read_b128 v[166:169], v96 offset:3072
	s_add_u32 s82, s26, 0x80000
	v_mov_b32_e32 v96, v152
	s_mov_b32 m0, s37
	ds_read_b128 v[170:173], v157 offset:32768
	ds_read_b128 v[174:177], v157 offset:33792
	ds_read_b128 v[178:181], v157 offset:34816
	ds_read_b128 v[182:185], v157 offset:35840
	ds_read_b128 v[186:189], v157 offset:36864
	ds_read_b128 v[190:193], v157 offset:37888
	ds_read_b128 v[194:197], v157 offset:38912
	ds_read_b128 v[198:201], v157 offset:39936
	s_addc_u32 s83, s27, 0
	s_nop 0
	global_load_lds_dwordx4 v96, s[82:83]
	v_mov_b32_e32 v96, v153
	s_mov_b32 m0, s38
	s_nop 0
	global_load_lds_dwordx4 v96, s[82:83]
	s_waitcnt vmcnt(8)
	s_nop 0
	s_barrier
	s_setprio 1
	s_waitcnt lgkmcnt(0)
	v_mfma_f32_16x16x32_bf16 v[126:129], v[130:133], v[170:173], v[126:129]
	v_mfma_f32_16x16x32_bf16 v[122:125], v[138:141], v[170:173], v[122:125]
	v_mfma_f32_16x16x32_bf16 v[114:117], v[130:133], v[178:181], v[114:117]
	v_mfma_f32_16x16x32_bf16 v[110:113], v[138:141], v[178:181], v[110:113]
	v_mfma_f32_16x16x32_bf16 v[98:101], v[130:133], v[186:189], v[98:101]
	v_mfma_f32_16x16x32_bf16 v[92:95], v[138:141], v[186:189], v[92:95]
	v_mfma_f32_16x16x32_bf16 v[80:83], v[130:133], v[194:197], v[80:83]
	v_mfma_f32_16x16x32_bf16 v[76:79], v[138:141], v[194:197], v[76:79]
	v_mfma_f32_16x16x32_bf16 v[126:129], v[134:137], v[174:177], v[126:129]
	v_mfma_f32_16x16x32_bf16 v[122:125], v[142:145], v[174:177], v[122:125]
	v_mfma_f32_16x16x32_bf16 v[114:117], v[134:137], v[182:185], v[114:117]
	v_mfma_f32_16x16x32_bf16 v[110:113], v[142:145], v[182:185], v[110:113]
	v_mfma_f32_16x16x32_bf16 v[98:101], v[134:137], v[190:193], v[98:101]
	v_mfma_f32_16x16x32_bf16 v[92:95], v[142:145], v[190:193], v[92:95]
	v_mfma_f32_16x16x32_bf16 v[80:83], v[134:137], v[198:201], v[80:83]
	v_mfma_f32_16x16x32_bf16 v[76:79], v[142:145], v[198:201], v[76:79]
	s_setprio 0
	s_setprio 1
	v_mfma_f32_16x16x32_bf16 v[118:121], v[146:149], v[170:173], v[118:121]
	v_mfma_f32_16x16x32_bf16 v[106:109], v[162:165], v[170:173], v[106:109]
	v_mfma_f32_16x16x32_bf16 v[102:105], v[146:149], v[178:181], v[102:105]
	v_mfma_f32_16x16x32_bf16 v[88:91], v[162:165], v[178:181], v[88:91]
	v_mfma_f32_16x16x32_bf16 v[84:87], v[146:149], v[186:189], v[84:87]
	v_mfma_f32_16x16x32_bf16 v[72:75], v[162:165], v[186:189], v[72:75]
	v_mfma_f32_16x16x32_bf16 v[68:71], v[146:149], v[194:197], v[68:71]
	v_mfma_f32_16x16x32_bf16 v[60:63], v[162:165], v[194:197], v[60:63]
	v_mfma_f32_16x16x32_bf16 v[118:121], v[158:161], v[174:177], v[118:121]
	v_mfma_f32_16x16x32_bf16 v[106:109], v[166:169], v[174:177], v[106:109]
	v_mfma_f32_16x16x32_bf16 v[102:105], v[158:161], v[182:185], v[102:105]
	v_mfma_f32_16x16x32_bf16 v[88:91], v[166:169], v[182:185], v[88:91]
	v_mfma_f32_16x16x32_bf16 v[84:87], v[158:161], v[190:193], v[84:87]
	v_mfma_f32_16x16x32_bf16 v[72:75], v[166:169], v[190:193], v[72:75]
	v_mfma_f32_16x16x32_bf16 v[68:71], v[158:161], v[198:201], v[68:71]
	v_mfma_f32_16x16x32_bf16 v[60:63], v[166:169], v[198:201], v[60:63]
	s_setprio 0
	s_barrier
	v_mov_b32_e32 v96, v152
	ds_read_b128 v[170:173], v157 offset:49152
	ds_read_b128 v[174:177], v157 offset:50176
	ds_read_b128 v[178:181], v157 offset:51200
	ds_read_b128 v[182:185], v157 offset:52224
	ds_read_b128 v[186:189], v157 offset:53248
	ds_read_b128 v[190:193], v157 offset:54272
	ds_read_b128 v[194:197], v157 offset:55296
	ds_read_b128 v[198:201], v157 offset:56320
	s_add_i32 s82, s84, s34
	v_lshl_add_u64 v[150:151], s[28:29], 0, v[96:97]
	v_lshl_add_u64 v[150:151], v[150:151], 0, s[0:1]
	s_mov_b32 m0, s82
	v_mov_b32_e32 v96, v153
	global_load_lds_dwordx4 v[150:151], off
	s_add_i32 m0, s82, 0x2000
	s_nop 0
	v_lshl_add_u64 v[150:151], s[28:29], 0, v[96:97]
	s_add_u32 s28, s28, 0x80080
	v_lshl_add_u64 v[150:151], v[150:151], 0, s[0:1]
	s_addc_u32 s29, s29, 0
	v_mov_b32_e32 v96, v152
	s_add_i32 s82, s85, s34
	global_load_lds_dwordx4 v[150:151], off
	s_mov_b32 m0, s82
	s_nop 0
	global_load_lds_dwordx4 v96, s[28:29]
	v_mov_b32_e32 v96, v153
	s_add_i32 m0, s82, 0x2000
	s_nop 0
	global_load_lds_dwordx4 v96, s[28:29]
	v_mov_b32_e32 v96, v152
	s_mov_b32 m0, s40
	v_lshl_add_u64 v[150:151], s[26:27], 0, v[96:97]
	v_lshl_add_u64 v[150:151], v[150:151], 0, s[0:1]
	v_mov_b32_e32 v96, v153
	global_load_lds_dwordx4 v[150:151], off
	s_mov_b32 m0, s41
	v_lshl_add_u64 v[150:151], s[26:27], 0, v[96:97]
	v_lshl_add_u64 v[150:151], v[150:151], 0, s[0:1]
	global_load_lds_dwordx4 v[150:151], off
	s_waitcnt vmcnt(8)
	s_nop 0
	s_barrier
	s_setprio 1
	s_waitcnt lgkmcnt(0)
	v_mfma_f32_16x16x32_bf16 v[64:67], v[130:133], v[170:173], v[64:67]
	v_mfma_f32_16x16x32_bf16 v[56:59], v[138:141], v[170:173], v[56:59]
	v_mfma_f32_16x16x32_bf16 v[48:51], v[130:133], v[178:181], v[48:51]
	v_mfma_f32_16x16x32_bf16 v[44:47], v[138:141], v[178:181], v[44:47]
	v_mfma_f32_16x16x32_bf16 v[32:35], v[130:133], v[186:189], v[32:35]
	v_mfma_f32_16x16x32_bf16 v[28:31], v[138:141], v[186:189], v[28:31]
	v_mfma_f32_16x16x32_bf16 v[16:19], v[130:133], v[194:197], v[16:19]
	v_mfma_f32_16x16x32_bf16 v[12:15], v[138:141], v[194:197], v[12:15]
	v_mfma_f32_16x16x32_bf16 v[64:67], v[134:137], v[174:177], v[64:67]
	v_mfma_f32_16x16x32_bf16 v[56:59], v[142:145], v[174:177], v[56:59]
	v_mfma_f32_16x16x32_bf16 v[48:51], v[134:137], v[182:185], v[48:51]
	v_mfma_f32_16x16x32_bf16 v[44:47], v[142:145], v[182:185], v[44:47]
	v_mfma_f32_16x16x32_bf16 v[32:35], v[134:137], v[190:193], v[32:35]
	v_mfma_f32_16x16x32_bf16 v[28:31], v[142:145], v[190:193], v[28:31]
	v_mfma_f32_16x16x32_bf16 v[16:19], v[134:137], v[198:201], v[16:19]
	v_mfma_f32_16x16x32_bf16 v[12:15], v[142:145], v[198:201], v[12:15]
	s_setprio 0
	s_setprio 1
	v_mfma_f32_16x16x32_bf16 v[52:55], v[146:149], v[170:173], v[52:55]
	v_mfma_f32_16x16x32_bf16 v[40:43], v[162:165], v[170:173], v[40:43]
	v_mfma_f32_16x16x32_bf16 v[36:39], v[146:149], v[178:181], v[36:39]
	v_mfma_f32_16x16x32_bf16 v[24:27], v[162:165], v[178:181], v[24:27]
	v_mfma_f32_16x16x32_bf16 v[20:23], v[146:149], v[186:189], v[20:23]
	v_mfma_f32_16x16x32_bf16 v[8:11], v[162:165], v[186:189], v[8:11]
	v_mfma_f32_16x16x32_bf16 v[4:7], v[146:149], v[194:197], v[4:7]
	v_mfma_f32_16x16x32_bf16 v[0:3], v[162:165], v[194:197], v[0:3]
	v_mfma_f32_16x16x32_bf16 v[52:55], v[158:161], v[174:177], v[52:55]
	v_mfma_f32_16x16x32_bf16 v[40:43], v[166:169], v[174:177], v[40:43]
	v_mfma_f32_16x16x32_bf16 v[36:39], v[158:161], v[182:185], v[36:39]
	v_mfma_f32_16x16x32_bf16 v[24:27], v[166:169], v[182:185], v[24:27]
	v_mfma_f32_16x16x32_bf16 v[20:23], v[158:161], v[190:193], v[20:23]
	v_mfma_f32_16x16x32_bf16 v[8:11], v[166:169], v[190:193], v[8:11]
	v_mfma_f32_16x16x32_bf16 v[4:7], v[158:161], v[198:201], v[4:7]
	v_mfma_f32_16x16x32_bf16 v[0:3], v[166:169], v[198:201], v[0:3]
	s_setprio 0
	s_barrier
	s_add_i32 s81, s81, 2
	s_add_u32 s79, s79, 0x100
	s_addc_u32 s80, s80, 0
	s_add_u32 s24, s24, 0x100
	s_addc_u32 s25, s25, 0
	s_cmp_gt_u32 s81, 29
	s_cbranch_scc0 .LBB0_1370
	s_and_b64 vcc, exec, s[14:15]
	s_cbranch_vccz .LBB0_1373
	s_barrier

.LBB0_1783:
	s_add_u32 s20, s18, 0xfff80080
	s_addc_u32 s21, s19, -1
	s_add_i32 s76, 0, 0x10000
	s_cmp_eq_u32 s47, 28
	s_cselect_b32 s21, s15, s21
	s_cselect_b32 s20, s14, s20
	v_add_u32_e32 v96, s76, v138
	s_cselect_b32 s23, s17, s46
	s_cselect_b32 s22, s16, s43
	s_add_i32 s80, 0, 0x14000
	ds_read_b128 v[142:145], v96
	ds_read_b128 v[146:149], v96 offset:1024
	ds_read_b128 v[150:153], v96 offset:2048
	ds_read_b128 v[154:157], v96 offset:3072
	v_add_u32_e32 v96, s80, v138
	ds_read_b128 v[158:161], v96
	ds_read_b128 v[162:165], v96 offset:1024
	ds_read_b128 v[166:169], v96 offset:2048
	ds_read_b128 v[170:173], v96 offset:3072
	v_mov_b32_e32 v96, v131
	ds_read_b128 v[174:177], v140
	ds_read_b128 v[178:181], v140 offset:1024
	ds_read_b128 v[182:185], v140 offset:2048
	ds_read_b128 v[186:189], v140 offset:3072
	ds_read_b128 v[190:193], v140 offset:4096
	ds_read_b128 v[194:197], v140 offset:5120
	ds_read_b128 v[198:201], v140 offset:6144
	ds_read_b128 v[202:205], v140 offset:7168
	s_add_i32 m0, s26, 0xc000
	s_nop 0
	global_load_lds_dwordx4 v96, s[18:19]
	v_mov_b32_e32 v96, v135
	s_add_i32 m0, s26, 0xe000
	s_nop 0
	global_load_lds_dwordx4 v96, s[18:19]
	s_waitcnt vmcnt(8)
	s_nop 0
	s_barrier
	s_setprio 1
	s_waitcnt lgkmcnt(0)
	v_mfma_f32_16x16x32_bf16 v[126:129], v[142:145], v[174:177], v[126:129]
	v_mfma_f32_16x16x32_bf16 v[118:121], v[150:153], v[174:177], v[118:121]
	v_mfma_f32_16x16x32_bf16 v[110:113], v[142:145], v[182:185], v[110:113]
	v_mfma_f32_16x16x32_bf16 v[102:105], v[150:153], v[182:185], v[102:105]
	v_mfma_f32_16x16x32_bf16 v[92:95], v[142:145], v[190:193], v[92:95]
	v_mfma_f32_16x16x32_bf16 v[84:87], v[150:153], v[190:193], v[84:87]
	v_mfma_f32_16x16x32_bf16 v[76:79], v[142:145], v[198:201], v[76:79]
	v_mfma_f32_16x16x32_bf16 v[68:71], v[150:153], v[198:201], v[68:71]
	v_mfma_f32_16x16x32_bf16 v[126:129], v[146:149], v[178:181], v[126:129]
	v_mfma_f32_16x16x32_bf16 v[118:121], v[154:157], v[178:181], v[118:121]
	v_mfma_f32_16x16x32_bf16 v[110:113], v[146:149], v[186:189], v[110:113]
	v_mfma_f32_16x16x32_bf16 v[102:105], v[154:157], v[186:189], v[102:105]
	v_mfma_f32_16x16x32_bf16 v[92:95], v[146:149], v[194:197], v[92:95]
	v_mfma_f32_16x16x32_bf16 v[84:87], v[154:157], v[194:197], v[84:87]
	v_mfma_f32_16x16x32_bf16 v[76:79], v[146:149], v[202:205], v[76:79]
	v_mfma_f32_16x16x32_bf16 v[68:71], v[154:157], v[202:205], v[68:71]
	s_setprio 0
	s_setprio 1
	v_mfma_f32_16x16x32_bf16 v[122:125], v[158:161], v[174:177], v[122:125]
	v_mfma_f32_16x16x32_bf16 v[114:117], v[166:169], v[174:177], v[114:117]
	v_mfma_f32_16x16x32_bf16 v[106:109], v[158:161], v[182:185], v[106:109]
	v_mfma_f32_16x16x32_bf16 v[98:101], v[166:169], v[182:185], v[98:101]
	v_mfma_f32_16x16x32_bf16 v[88:91], v[158:161], v[190:193], v[88:91]
	v_mfma_f32_16x16x32_bf16 v[80:83], v[166:169], v[190:193], v[80:83]
	v_mfma_f32_16x16x32_bf16 v[72:75], v[158:161], v[198:201], v[72:75]
	v_mfma_f32_16x16x32_bf16 v[64:67], v[166:169], v[198:201], v[64:67]
	v_mfma_f32_16x16x32_bf16 v[122:125], v[162:165], v[178:181], v[122:125]
	v_mfma_f32_16x16x32_bf16 v[114:117], v[170:173], v[178:181], v[114:117]
	v_mfma_f32_16x16x32_bf16 v[106:109], v[162:165], v[186:189], v[106:109]
	v_mfma_f32_16x16x32_bf16 v[98:101], v[170:173], v[186:189], v[98:101]
	v_mfma_f32_16x16x32_bf16 v[88:91], v[162:165], v[194:197], v[88:91]
	v_mfma_f32_16x16x32_bf16 v[80:83], v[170:173], v[194:197], v[80:83]
	v_mfma_f32_16x16x32_bf16 v[72:75], v[162:165], v[202:205], v[72:75]
	v_mfma_f32_16x16x32_bf16 v[64:67], v[170:173], v[202:205], v[64:67]
	s_setprio 0
	s_barrier
	v_mov_b32_e32 v96, v134
	s_add_i32 s76, s76, s25
	ds_read_b128 v[174:177], v140 offset:16384
	ds_read_b128 v[178:181], v140 offset:17408
	ds_read_b128 v[182:185], v140 offset:18432
	ds_read_b128 v[186:189], v140 offset:19456
	ds_read_b128 v[190:193], v140 offset:20480
	ds_read_b128 v[194:197], v140 offset:21504
	ds_read_b128 v[198:201], v140 offset:22528
	ds_read_b128 v[202:205], v140 offset:23552
	s_mov_b32 m0, s76
	s_nop 0
	global_load_lds_dwordx4 v96, s[22:23]
	v_mov_b32_e32 v96, v136
	s_add_i32 m0, s76, 0x2000
	s_add_u32 s78, s22, 0x80000
	global_load_lds_dwordx4 v96, s[22:23]
	s_addc_u32 s79, s23, 0
	v_mov_b32_e32 v96, v134
	s_add_i32 s76, s80, s25
	s_mov_b32 m0, s76
	s_nop 0
	global_load_lds_dwordx4 v96, s[78:79]
	v_mov_b32_e32 v96, v136
	s_add_i32 m0, s76, 0x2000
	s_nop 0
	global_load_lds_dwordx4 v96, s[78:79]
	v_mov_b32_e32 v96, v131
	s_mov_b32 m0, s26
	s_nop 0
	global_load_lds_dwordx4 v96, s[20:21]
	v_mov_b32_e32 v96, v135
	s_mov_b32 m0, s27
	s_nop 0
	global_load_lds_dwordx4 v96, s[20:21]
	s_waitcnt vmcnt(8)
	s_nop 0
	s_barrier
	s_setprio 1
	s_waitcnt lgkmcnt(0)
	v_mfma_f32_16x16x32_bf16 v[60:63], v[142:145], v[174:177], v[60:63]
	v_mfma_f32_16x16x32_bf16 v[52:55], v[150:153], v[174:177], v[52:55]
	v_mfma_f32_16x16x32_bf16 v[44:47], v[142:145], v[182:185], v[44:47]
	v_mfma_f32_16x16x32_bf16 v[36:39], v[150:153], v[182:185], v[36:39]
	v_mfma_f32_16x16x32_bf16 v[28:31], v[142:145], v[190:193], v[28:31]
	v_mfma_f32_16x16x32_bf16 v[20:23], v[150:153], v[190:193], v[20:23]
	v_mfma_f32_16x16x32_bf16 v[12:15], v[142:145], v[198:201], v[12:15]
	v_mfma_f32_16x16x32_bf16 v[4:7], v[150:153], v[198:201], v[4:7]
	v_mfma_f32_16x16x32_bf16 v[60:63], v[146:149], v[178:181], v[60:63]
	v_mfma_f32_16x16x32_bf16 v[52:55], v[154:157], v[178:181], v[52:55]
	v_mfma_f32_16x16x32_bf16 v[44:47], v[146:149], v[186:189], v[44:47]
	v_mfma_f32_16x16x32_bf16 v[36:39], v[154:157], v[186:189], v[36:39]
	v_mfma_f32_16x16x32_bf16 v[28:31], v[146:149], v[194:197], v[28:31]
	v_mfma_f32_16x16x32_bf16 v[20:23], v[154:157], v[194:197], v[20:23]
	v_mfma_f32_16x16x32_bf16 v[12:15], v[146:149], v[202:205], v[12:15]
	v_mfma_f32_16x16x32_bf16 v[4:7], v[154:157], v[202:205], v[4:7]
	s_setprio 0
	s_setprio 1
	v_mfma_f32_16x16x32_bf16 v[56:59], v[158:161], v[174:177], v[56:59]
	v_mfma_f32_16x16x32_bf16 v[48:51], v[166:169], v[174:177], v[48:51]
	v_mfma_f32_16x16x32_bf16 v[40:43], v[158:161], v[182:185], v[40:43]
	v_mfma_f32_16x16x32_bf16 v[32:35], v[166:169], v[182:185], v[32:35]
	v_mfma_f32_16x16x32_bf16 v[24:27], v[158:161], v[190:193], v[24:27]
	v_mfma_f32_16x16x32_bf16 v[16:19], v[166:169], v[190:193], v[16:19]
	v_mfma_f32_16x16x32_bf16 v[8:11], v[158:161], v[198:201], v[8:11]
	v_mfma_f32_16x16x32_bf16 v[0:3], v[166:169], v[198:201], v[0:3]
	v_mfma_f32_16x16x32_bf16 v[56:59], v[162:165], v[178:181], v[56:59]
	v_mfma_f32_16x16x32_bf16 v[48:51], v[170:173], v[178:181], v[48:51]
	v_mfma_f32_16x16x32_bf16 v[40:43], v[162:165], v[186:189], v[40:43]
	v_mfma_f32_16x16x32_bf16 v[32:35], v[170:173], v[186:189], v[32:35]
	v_mfma_f32_16x16x32_bf16 v[24:27], v[162:165], v[194:197], v[24:27]
	v_mfma_f32_16x16x32_bf16 v[16:19], v[170:173], v[194:197], v[16:19]
	v_mfma_f32_16x16x32_bf16 v[8:11], v[162:165], v[202:205], v[8:11]
	v_mfma_f32_16x16x32_bf16 v[0:3], v[170:173], v[202:205], v[0:3]
	s_setprio 0
	s_barrier
	s_add_i32 s76, 0, 0x18000
	v_add_u32_e32 v96, s76, v138
	s_add_i32 s80, 0, 0x1c000
	ds_read_b128 v[142:145], v96
	ds_read_b128 v[146:149], v96 offset:1024
	ds_read_b128 v[150:153], v96 offset:2048
	ds_read_b128 v[154:157], v96 offset:3072
	v_add_u32_e32 v96, s80, v138
	ds_read_b128 v[158:161], v96
	ds_read_b128 v[162:165], v96 offset:1024
	ds_read_b128 v[166:169], v96 offset:2048
	ds_read_b128 v[170:173], v96 offset:3072
	s_add_u32 s78, s20, 0x80000
	v_mov_b32_e32 v96, v131
	s_mov_b32 m0, s28
	ds_read_b128 v[174:177], v140 offset:32768
	ds_read_b128 v[178:181], v140 offset:33792
	ds_read_b128 v[182:185], v140 offset:34816
	ds_read_b128 v[186:189], v140 offset:35840
	ds_read_b128 v[190:193], v140 offset:36864
	ds_read_b128 v[194:197], v140 offset:37888
	ds_read_b128 v[198:201], v140 offset:38912
	ds_read_b128 v[202:205], v140 offset:39936
	s_addc_u32 s79, s21, 0
	s_nop 0
	global_load_lds_dwordx4 v96, s[78:79]
	v_mov_b32_e32 v96, v135
	s_mov_b32 m0, s29
	s_nop 0
	global_load_lds_dwordx4 v96, s[78:79]
	s_waitcnt vmcnt(8)
	s_nop 0
	s_barrier
	s_setprio 1
	s_waitcnt lgkmcnt(0)
	v_mfma_f32_16x16x32_bf16 v[126:129], v[142:145], v[174:177], v[126:129]
	v_mfma_f32_16x16x32_bf16 v[118:121], v[150:153], v[174:177], v[118:121]
	v_mfma_f32_16x16x32_bf16 v[110:113], v[142:145], v[182:185], v[110:113]
	v_mfma_f32_16x16x32_bf16 v[102:105], v[150:153], v[182:185], v[102:105]
	v_mfma_f32_16x16x32_bf16 v[92:95], v[142:145], v[190:193], v[92:95]
	v_mfma_f32_16x16x32_bf16 v[84:87], v[150:153], v[190:193], v[84:87]
	v_mfma_f32_16x16x32_bf16 v[76:79], v[142:145], v[198:201], v[76:79]
	v_mfma_f32_16x16x32_bf16 v[68:71], v[150:153], v[198:201], v[68:71]
	v_mfma_f32_16x16x32_bf16 v[126:129], v[146:149], v[178:181], v[126:129]
	v_mfma_f32_16x16x32_bf16 v[118:121], v[154:157], v[178:181], v[118:121]
	v_mfma_f32_16x16x32_bf16 v[110:113], v[146:149], v[186:189], v[110:113]
	v_mfma_f32_16x16x32_bf16 v[102:105], v[154:157], v[186:189], v[102:105]
	v_mfma_f32_16x16x32_bf16 v[92:95], v[146:149], v[194:197], v[92:95]
	v_mfma_f32_16x16x32_bf16 v[84:87], v[154:157], v[194:197], v[84:87]
	v_mfma_f32_16x16x32_bf16 v[76:79], v[146:149], v[202:205], v[76:79]
	v_mfma_f32_16x16x32_bf16 v[68:71], v[154:157], v[202:205], v[68:71]
	s_setprio 0
	s_setprio 1
	v_mfma_f32_16x16x32_bf16 v[122:125], v[158:161], v[174:177], v[122:125]
	v_mfma_f32_16x16x32_bf16 v[114:117], v[166:169], v[174:177], v[114:117]
	v_mfma_f32_16x16x32_bf16 v[106:109], v[158:161], v[182:185], v[106:109]
	v_mfma_f32_16x16x32_bf16 v[98:101], v[166:169], v[182:185], v[98:101]
	v_mfma_f32_16x16x32_bf16 v[88:91], v[158:161], v[190:193], v[88:91]
	v_mfma_f32_16x16x32_bf16 v[80:83], v[166:169], v[190:193], v[80:83]
	v_mfma_f32_16x16x32_bf16 v[72:75], v[158:161], v[198:201], v[72:75]
	v_mfma_f32_16x16x32_bf16 v[64:67], v[166:169], v[198:201], v[64:67]
	v_mfma_f32_16x16x32_bf16 v[122:125], v[162:165], v[178:181], v[122:125]
	v_mfma_f32_16x16x32_bf16 v[114:117], v[170:173], v[178:181], v[114:117]
	v_mfma_f32_16x16x32_bf16 v[106:109], v[162:165], v[186:189], v[106:109]
	v_mfma_f32_16x16x32_bf16 v[98:101], v[170:173], v[186:189], v[98:101]
	v_mfma_f32_16x16x32_bf16 v[88:91], v[162:165], v[194:197], v[88:91]
	v_mfma_f32_16x16x32_bf16 v[80:83], v[170:173], v[194:197], v[80:83]
	v_mfma_f32_16x16x32_bf16 v[72:75], v[162:165], v[202:205], v[72:75]
	v_mfma_f32_16x16x32_bf16 v[64:67], v[170:173], v[202:205], v[64:67]
	s_setprio 0
	s_barrier
	v_mov_b32_e32 v96, v134
	ds_read_b128 v[174:177], v140 offset:49152
	ds_read_b128 v[178:181], v140 offset:50176
	ds_read_b128 v[182:185], v140 offset:51200
	ds_read_b128 v[186:189], v140 offset:52224
	ds_read_b128 v[190:193], v140 offset:53248
	ds_read_b128 v[194:197], v140 offset:54272
	ds_read_b128 v[198:201], v140 offset:55296
	ds_read_b128 v[202:205], v140 offset:56320
	s_add_i32 s76, s76, s25
	v_lshl_add_u64 v[132:133], s[22:23], 0, v[96:97]
	v_lshl_add_u64 v[132:133], v[132:133], 0, s[0:1]
	s_mov_b32 m0, s76
	v_mov_b32_e32 v96, v136
	global_load_lds_dwordx4 v[132:133], off
	s_add_i32 m0, s76, 0x2000
	s_nop 0
	v_lshl_add_u64 v[132:133], s[22:23], 0, v[96:97]
	s_add_u32 s22, s22, 0x80080
	v_lshl_add_u64 v[132:133], v[132:133], 0, s[0:1]
	s_addc_u32 s23, s23, 0
	v_mov_b32_e32 v96, v134
	s_add_i32 s76, s80, s25
	global_load_lds_dwordx4 v[132:133], off
	s_mov_b32 m0, s76
	s_nop 0
	global_load_lds_dwordx4 v96, s[22:23]
	v_mov_b32_e32 v96, v136
	s_add_i32 m0, s76, 0x2000
	s_nop 0
	global_load_lds_dwordx4 v96, s[22:23]
	v_mov_b32_e32 v96, v131
	s_mov_b32 m0, s31
	v_lshl_add_u64 v[132:133], s[20:21], 0, v[96:97]
	v_lshl_add_u64 v[132:133], v[132:133], 0, s[0:1]
	v_mov_b32_e32 v96, v135
	global_load_lds_dwordx4 v[132:133], off
	s_mov_b32 m0, s35
	v_lshl_add_u64 v[132:133], s[20:21], 0, v[96:97]
	v_lshl_add_u64 v[132:133], v[132:133], 0, s[0:1]
	global_load_lds_dwordx4 v[132:133], off
	s_waitcnt vmcnt(8)
	s_nop 0
	s_barrier
	s_setprio 1
	s_waitcnt lgkmcnt(0)
	v_mfma_f32_16x16x32_bf16 v[60:63], v[142:145], v[174:177], v[60:63]
	v_mfma_f32_16x16x32_bf16 v[52:55], v[150:153], v[174:177], v[52:55]
	v_mfma_f32_16x16x32_bf16 v[44:47], v[142:145], v[182:185], v[44:47]
	v_mfma_f32_16x16x32_bf16 v[36:39], v[150:153], v[182:185], v[36:39]
	v_mfma_f32_16x16x32_bf16 v[28:31], v[142:145], v[190:193], v[28:31]
	v_mfma_f32_16x16x32_bf16 v[20:23], v[150:153], v[190:193], v[20:23]
	v_mfma_f32_16x16x32_bf16 v[12:15], v[142:145], v[198:201], v[12:15]
	v_mfma_f32_16x16x32_bf16 v[4:7], v[150:153], v[198:201], v[4:7]
	v_mfma_f32_16x16x32_bf16 v[60:63], v[146:149], v[178:181], v[60:63]
	v_mfma_f32_16x16x32_bf16 v[52:55], v[154:157], v[178:181], v[52:55]
	v_mfma_f32_16x16x32_bf16 v[44:47], v[146:149], v[186:189], v[44:47]
	v_mfma_f32_16x16x32_bf16 v[36:39], v[154:157], v[186:189], v[36:39]
	v_mfma_f32_16x16x32_bf16 v[28:31], v[146:149], v[194:197], v[28:31]
	v_mfma_f32_16x16x32_bf16 v[20:23], v[154:157], v[194:197], v[20:23]
	v_mfma_f32_16x16x32_bf16 v[12:15], v[146:149], v[202:205], v[12:15]
	v_mfma_f32_16x16x32_bf16 v[4:7], v[154:157], v[202:205], v[4:7]
	s_setprio 0
	s_setprio 1
	v_mfma_f32_16x16x32_bf16 v[56:59], v[158:161], v[174:177], v[56:59]
	v_mfma_f32_16x16x32_bf16 v[48:51], v[166:169], v[174:177], v[48:51]
	v_mfma_f32_16x16x32_bf16 v[40:43], v[158:161], v[182:185], v[40:43]
	v_mfma_f32_16x16x32_bf16 v[32:35], v[166:169], v[182:185], v[32:35]
	v_mfma_f32_16x16x32_bf16 v[24:27], v[158:161], v[190:193], v[24:27]
	v_mfma_f32_16x16x32_bf16 v[16:19], v[166:169], v[190:193], v[16:19]
	v_mfma_f32_16x16x32_bf16 v[8:11], v[158:161], v[198:201], v[8:11]
	v_mfma_f32_16x16x32_bf16 v[0:3], v[166:169], v[198:201], v[0:3]
	v_mfma_f32_16x16x32_bf16 v[56:59], v[162:165], v[178:181], v[56:59]
	v_mfma_f32_16x16x32_bf16 v[48:51], v[170:173], v[178:181], v[48:51]
	v_mfma_f32_16x16x32_bf16 v[40:43], v[162:165], v[186:189], v[40:43]
	v_mfma_f32_16x16x32_bf16 v[32:35], v[170:173], v[186:189], v[32:35]
	v_mfma_f32_16x16x32_bf16 v[24:27], v[162:165], v[194:197], v[24:27]
	v_mfma_f32_16x16x32_bf16 v[16:19], v[170:173], v[194:197], v[16:19]
	v_mfma_f32_16x16x32_bf16 v[8:11], v[162:165], v[202:205], v[8:11]
	v_mfma_f32_16x16x32_bf16 v[0:3], v[170:173], v[202:205], v[0:3]
	s_setprio 0
	s_barrier
	s_add_i32 s47, s47, 2
	s_add_u32 s43, s43, 0x100
	s_addc_u32 s46, s46, 0
	s_add_u32 s18, s18, 0x100
	s_addc_u32 s19, s19, 0
	s_cmp_gt_u32 s47, 29
	s_cbranch_scc0 .LBB0_1783
	s_and_b64 vcc, exec, s[8:9]
	s_cbranch_vccz .LBB0_1786
	s_barrier

.LBB0_1956:
	s_add_u32 s24, s22, 0xfff50080
	s_addc_u32 s25, s23, -1
	s_add_i32 s80, 0, 0x10000
	s_cmp_eq_u32 s79, 40
	s_cselect_b32 s25, s19, s25
	s_cselect_b32 s24, s18, s24
	v_add_u32_e32 v96, s80, v156
	s_cselect_b32 s27, s21, s78
	s_cselect_b32 s26, s20, s76
	s_add_i32 s82, 0, 0x14000
	ds_read_b128 v[132:135], v96
	ds_read_b128 v[136:139], v96 offset:1024
	ds_read_b128 v[140:143], v96 offset:2048
	ds_read_b128 v[144:147], v96 offset:3072
	v_add_u32_e32 v96, s82, v156
	ds_read_b128 v[160:163], v96
	ds_read_b128 v[164:167], v96 offset:1024
	ds_read_b128 v[168:171], v96 offset:2048
	ds_read_b128 v[172:175], v96 offset:3072
	v_mov_b32_e32 v96, v131
	ds_read_b128 v[176:179], v158
	ds_read_b128 v[180:183], v158 offset:1024
	ds_read_b128 v[184:187], v158 offset:2048
	ds_read_b128 v[188:191], v158 offset:3072
	ds_read_b128 v[192:195], v158 offset:4096
	ds_read_b128 v[196:199], v158 offset:5120
	ds_read_b128 v[222:225], v158 offset:6144
	ds_read_b128 v[226:229], v158 offset:7168
	s_add_i32 m0, s30, 0xc000
	s_nop 0
	global_load_lds_dwordx4 v96, s[22:23]
	v_mov_b32_e32 v96, v154
	s_add_i32 m0, s30, 0xe000
	s_nop 0
	global_load_lds_dwordx4 v96, s[22:23]
	s_waitcnt vmcnt(8)
	s_nop 0
	s_barrier
	s_setprio 1
	s_waitcnt lgkmcnt(0)
	v_mfma_f32_16x16x128_f8f6f4 v[126:129], v[132:139], v[176:183], v[126:129]
	v_mfma_f32_16x16x128_f8f6f4 v[122:125], v[140:147], v[176:183], v[122:125]
	v_mfma_f32_16x16x128_f8f6f4 v[110:113], v[132:139], v[184:191], v[110:113]
	v_mfma_f32_16x16x128_f8f6f4 v[106:109], v[140:147], v[184:191], v[106:109]
	v_mfma_f32_16x16x128_f8f6f4 v[148:151], v[132:139], v[192:199], v[92:95]
	v_mfma_f32_16x16x128_f8f6f4 v[200:203], v[140:147], v[192:199], v[88:91]
	v_mfma_f32_16x16x128_f8f6f4 v[204:207], v[132:139], v[222:229], v[76:79]
	v_mfma_f32_16x16x128_f8f6f4 v[208:211], v[140:147], v[222:229], v[72:75]
	s_setprio 0
	s_setprio 1
	v_mfma_f32_16x16x128_f8f6f4 v[118:121], v[160:167], v[176:183], v[118:121]
	v_mfma_f32_16x16x128_f8f6f4 v[114:117], v[168:175], v[176:183], v[114:117]
	v_mfma_f32_16x16x128_f8f6f4 v[102:105], v[160:167], v[184:191], v[102:105]
	v_mfma_f32_16x16x128_f8f6f4 v[98:101], v[168:175], v[184:191], v[98:101]
	v_mfma_f32_16x16x128_f8f6f4 v[176:179], v[160:167], v[192:199], v[84:87]
	v_mfma_f32_16x16x128_f8f6f4 v[180:183], v[168:175], v[192:199], v[80:83]
	v_mfma_f32_16x16x128_f8f6f4 v[184:187], v[160:167], v[222:229], v[68:71]
	v_mfma_f32_16x16x128_f8f6f4 v[188:191], v[168:175], v[222:229], v[64:67]
	s_setprio 0
	s_barrier
	v_mov_b32_e32 v96, v131
	s_add_i32 s80, s80, s29
	s_nop 2
	ds_read_b128 v[64:67], v158 offset:16384
	ds_read_b128 v[68:71], v158 offset:17408
	ds_read_b128 v[72:75], v158 offset:18432
	ds_read_b128 v[76:79], v158 offset:19456
	ds_read_b128 v[80:83], v158 offset:20480
	ds_read_b128 v[84:87], v158 offset:21504
	ds_read_b128 v[88:91], v158 offset:22528
	ds_read_b128 v[92:95], v158 offset:23552
	s_mov_b32 m0, s80
	s_nop 0
	global_load_lds_dwordx4 v96, s[26:27]
	v_mov_b32_e32 v96, v154
	s_add_i32 m0, s80, 0x2000
	s_add_u32 s80, s26, 0xb0000
	global_load_lds_dwordx4 v96, s[26:27]
	s_addc_u32 s81, s27, 0
	v_mov_b32_e32 v96, v131
	s_add_i32 s82, s82, s29
	s_mov_b32 m0, s82
	s_nop 0
	global_load_lds_dwordx4 v96, s[80:81]
	v_mov_b32_e32 v96, v154
	s_add_i32 m0, s82, 0x2000
	s_nop 0
	global_load_lds_dwordx4 v96, s[80:81]
	v_mov_b32_e32 v96, v131
	s_mov_b32 m0, s30
	s_nop 0
	global_load_lds_dwordx4 v96, s[24:25]
	v_mov_b32_e32 v96, v154
	s_mov_b32 m0, s31
	s_nop 0
	global_load_lds_dwordx4 v96, s[24:25]
	s_waitcnt vmcnt(8)
	s_nop 0
	s_barrier
	s_setprio 1
	s_waitcnt lgkmcnt(0)
	v_mfma_f32_16x16x128_f8f6f4 v[60:63], v[132:139], v[64:71], v[60:63]
	v_mfma_f32_16x16x128_f8f6f4 v[56:59], v[140:147], v[64:71], v[56:59]
	v_mfma_f32_16x16x128_f8f6f4 v[192:195], v[132:139], v[72:79], v[44:47]
	v_mfma_f32_16x16x128_f8f6f4 v[196:199], v[140:147], v[72:79], v[40:43]
	v_mfma_f32_16x16x128_f8f6f4 v[212:215], v[132:139], v[80:87], v[28:31]
	v_mfma_f32_16x16x128_f8f6f4 v[218:221], v[140:147], v[80:87], v[24:27]
	v_mfma_f32_16x16x128_f8f6f4 v[222:225], v[132:139], v[88:95], v[12:15]
	v_mfma_f32_16x16x128_f8f6f4 v[226:229], v[140:147], v[88:95], v[8:11]
	s_setprio 0
	s_setprio 1
	v_mfma_f32_16x16x128_f8f6f4 v[52:55], v[160:167], v[64:71], v[52:55]
	v_mfma_f32_16x16x128_f8f6f4 v[48:51], v[168:175], v[64:71], v[48:51]
	v_mfma_f32_16x16x128_f8f6f4 v[230:233], v[160:167], v[72:79], v[36:39]
	v_mfma_f32_16x16x128_f8f6f4 v[234:237], v[168:175], v[72:79], v[32:35]
	v_mfma_f32_16x16x128_f8f6f4 v[238:241], v[160:167], v[80:87], v[20:23]
	v_mfma_f32_16x16x128_f8f6f4 v[242:245], v[168:175], v[80:87], v[16:19]
	v_mfma_f32_16x16x128_f8f6f4 v[246:249], v[160:167], v[88:95], v[4:7]
	v_mfma_f32_16x16x128_f8f6f4 v[250:253], v[168:175], v[88:95], v[0:3]
	s_setprio 0
	s_barrier
	s_add_i32 s82, 0, 0x18000
	v_add_u32_e32 v8, s82, v156
	s_add_i32 s83, 0, 0x1c000
	s_nop 1
	ds_read_b128 v[0:3], v8
	ds_read_b128 v[4:7], v8 offset:1024
	ds_read_b128 v[16:19], v8 offset:2048
	ds_read_b128 v[20:23], v8 offset:3072
	v_add_u32_e32 v8, s83, v156
	ds_read_b128 v[132:135], v8
	ds_read_b128 v[136:139], v8 offset:1024
	ds_read_b128 v[140:143], v8 offset:2048
	ds_read_b128 v[144:147], v8 offset:3072
	s_add_u32 s80, s24, 0xb0000
	v_mov_b32_e32 v64, v131
	s_mov_b32 m0, s35
	ds_read_b128 v[8:11], v158 offset:32768
	ds_read_b128 v[12:15], v158 offset:33792
	ds_read_b128 v[24:27], v158 offset:34816
	ds_read_b128 v[28:31], v158 offset:35840
	ds_read_b128 v[32:35], v158 offset:36864
	ds_read_b128 v[36:39], v158 offset:37888
	ds_read_b128 v[40:43], v158 offset:38912
	ds_read_b128 v[44:47], v158 offset:39936
	s_addc_u32 s81, s25, 0
	s_nop 0
	global_load_lds_dwordx4 v64, s[80:81]
	v_mov_b32_e32 v64, v154
	s_mov_b32 m0, s36
	s_nop 0
	global_load_lds_dwordx4 v64, s[80:81]
	s_waitcnt vmcnt(8)
	s_nop 0
	s_barrier
	s_setprio 1
	s_waitcnt lgkmcnt(0)
	v_mfma_f32_16x16x128_f8f6f4 v[126:129], v[0:7], v[8:15], v[126:129]
	v_mfma_f32_16x16x128_f8f6f4 v[122:125], v[16:23], v[8:15], v[122:125]
	v_mfma_f32_16x16x128_f8f6f4 v[110:113], v[0:7], v[24:31], v[110:113]
	v_mfma_f32_16x16x128_f8f6f4 v[106:109], v[16:23], v[24:31], v[106:109]
	v_mfma_f32_16x16x128_f8f6f4 v[92:95], v[0:7], v[32:39], v[148:151]
	v_mfma_f32_16x16x128_f8f6f4 v[88:91], v[16:23], v[32:39], v[200:203]
	v_mfma_f32_16x16x128_f8f6f4 v[76:79], v[0:7], v[40:47], v[204:207]
	v_mfma_f32_16x16x128_f8f6f4 v[72:75], v[16:23], v[40:47], v[208:211]
	s_setprio 0
	s_setprio 1
	v_mfma_f32_16x16x128_f8f6f4 v[118:121], v[132:139], v[8:15], v[118:121]
	v_mfma_f32_16x16x128_f8f6f4 v[114:117], v[140:147], v[8:15], v[114:117]
	v_mfma_f32_16x16x128_f8f6f4 v[102:105], v[132:139], v[24:31], v[102:105]
	v_mfma_f32_16x16x128_f8f6f4 v[98:101], v[140:147], v[24:31], v[98:101]
	v_mfma_f32_16x16x128_f8f6f4 v[84:87], v[132:139], v[32:39], v[176:179]
	v_mfma_f32_16x16x128_f8f6f4 v[80:83], v[140:147], v[32:39], v[180:183]
	v_mfma_f32_16x16x128_f8f6f4 v[68:71], v[132:139], v[40:47], v[184:187]
	v_mfma_f32_16x16x128_f8f6f4 v[64:67], v[140:147], v[40:47], v[188:191]
	s_setprio 0
	s_barrier
	v_mov_b32_e32 v96, v131
	ds_read_b128 v[32:35], v158 offset:49152
	ds_read_b128 v[36:39], v158 offset:50176
	ds_read_b128 v[160:163], v158 offset:51200
	ds_read_b128 v[164:167], v158 offset:52224
	ds_read_b128 v[168:171], v158 offset:53248
	ds_read_b128 v[172:175], v158 offset:54272
	ds_read_b128 v[176:179], v158 offset:55296
	ds_read_b128 v[180:183], v158 offset:56320
	s_add_i32 s80, s82, s29
	v_lshl_add_u64 v[8:9], s[26:27], 0, v[96:97]
	v_lshl_add_u64 v[8:9], v[8:9], 0, s[0:1]
	s_mov_b32 m0, s80
	v_mov_b32_e32 v96, v154
	global_load_lds_dwordx4 v[8:9], off
	s_add_i32 m0, s80, 0x2000
	v_lshl_add_u64 v[8:9], s[26:27], 0, v[96:97]
	v_lshl_add_u64 v[8:9], v[8:9], 0, s[0:1]
	s_add_u32 s26, s26, 0xb0080
	global_load_lds_dwordx4 v[8:9], off
	s_addc_u32 s27, s27, 0
	v_mov_b32_e32 v8, v131
	s_add_i32 s80, s83, s29
	s_mov_b32 m0, s80
	v_mov_b32_e32 v96, v131
	global_load_lds_dwordx4 v8, s[26:27]
	v_mov_b32_e32 v8, v154
	s_add_i32 m0, s80, 0x2000
	s_nop 0
	global_load_lds_dwordx4 v8, s[26:27]
	s_mov_b32 m0, s37
	v_lshl_add_u64 v[8:9], s[24:25], 0, v[96:97]
	v_lshl_add_u64 v[8:9], v[8:9], 0, s[0:1]
	v_mov_b32_e32 v96, v154
	global_load_lds_dwordx4 v[8:9], off
	s_mov_b32 m0, s38
	v_lshl_add_u64 v[8:9], s[24:25], 0, v[96:97]
	v_lshl_add_u64 v[8:9], v[8:9], 0, s[0:1]
	global_load_lds_dwordx4 v[8:9], off
	s_waitcnt vmcnt(8)
	s_nop 0
	s_barrier
	s_setprio 1
	s_waitcnt lgkmcnt(0)
	v_mfma_f32_16x16x128_f8f6f4 v[60:63], v[0:7], v[32:39], v[60:63]
	v_mfma_f32_16x16x128_f8f6f4 v[56:59], v[16:23], v[32:39], v[56:59]
	v_mfma_f32_16x16x128_f8f6f4 v[44:47], v[0:7], v[160:167], v[192:195]
	v_mfma_f32_16x16x128_f8f6f4 v[40:43], v[16:23], v[160:167], v[196:199]
	v_mfma_f32_16x16x128_f8f6f4 v[28:31], v[0:7], v[168:175], v[212:215]
	v_mfma_f32_16x16x128_f8f6f4 v[24:27], v[16:23], v[168:175], v[218:221]
	v_mfma_f32_16x16x128_f8f6f4 v[12:15], v[0:7], v[176:183], v[222:225]
	v_mfma_f32_16x16x128_f8f6f4 v[8:11], v[16:23], v[176:183], v[226:229]
	s_setprio 0
	s_setprio 1
	v_mfma_f32_16x16x128_f8f6f4 v[52:55], v[132:139], v[32:39], v[52:55]
	v_mfma_f32_16x16x128_f8f6f4 v[48:51], v[140:147], v[32:39], v[48:51]
	v_mfma_f32_16x16x128_f8f6f4 v[36:39], v[132:139], v[160:167], v[230:233]
	v_mfma_f32_16x16x128_f8f6f4 v[32:35], v[140:147], v[160:167], v[234:237]
	v_mfma_f32_16x16x128_f8f6f4 v[20:23], v[132:139], v[168:175], v[238:241]
	v_mfma_f32_16x16x128_f8f6f4 v[16:19], v[140:147], v[168:175], v[242:245]
	v_mfma_f32_16x16x128_f8f6f4 v[4:7], v[132:139], v[176:183], v[246:249]
	v_mfma_f32_16x16x128_f8f6f4 v[0:3], v[140:147], v[176:183], v[250:253]
	s_setprio 0
	s_barrier
	s_add_i32 s79, s79, 2
	s_add_u32 s76, s76, 0x100
	s_addc_u32 s78, s78, 0
	s_add_u32 s22, s22, 0x100
	s_addc_u32 s23, s23, 0
	s_cmp_gt_u32 s79, 41
	s_cbranch_scc0 .LBB0_1956
	s_and_b64 vcc, exec, s[10:11]
	s_cbranch_vccz .LBB0_1959
	s_barrier

.LBB0_2129:
	s_add_u32 s18, s16, 0xfffc0080
	s_addc_u32 s19, s17, -1
	s_add_i32 s42, 0, 0x10000
	s_cmp_eq_u32 s41, 12
	s_cselect_b32 s19, s13, s19
	s_cselect_b32 s18, s12, s18
	v_add_u32_e32 v96, s42, v137
	s_cselect_b32 s21, s15, s40
	s_cselect_b32 s20, s14, s39
	s_add_i32 s46, 0, 0x14000
	ds_read_b128 v[140:143], v96
	ds_read_b128 v[144:147], v96 offset:1024
	ds_read_b128 v[148:151], v96 offset:2048
	ds_read_b128 v[152:155], v96 offset:3072
	v_add_u32_e32 v96, s46, v137
	ds_read_b128 v[156:159], v96
	ds_read_b128 v[160:163], v96 offset:1024
	ds_read_b128 v[164:167], v96 offset:2048
	ds_read_b128 v[168:171], v96 offset:3072
	v_mov_b32_e32 v96, v132
	ds_read_b128 v[172:175], v139
	ds_read_b128 v[176:179], v139 offset:1024
	ds_read_b128 v[180:183], v139 offset:2048
	ds_read_b128 v[184:187], v139 offset:3072
	ds_read_b128 v[188:191], v139 offset:4096
	ds_read_b128 v[192:195], v139 offset:5120
	ds_read_b128 v[196:199], v139 offset:6144
	ds_read_b128 v[200:203], v139 offset:7168
	s_add_i32 m0, s24, 0xc000
	s_nop 0
	global_load_lds_dwordx4 v96, s[16:17]
	v_mov_b32_e32 v96, v134
	s_add_i32 m0, s24, 0xe000
	s_nop 0
	global_load_lds_dwordx4 v96, s[16:17]
	s_waitcnt vmcnt(8)
	s_nop 0
	s_barrier
	s_setprio 1
	s_waitcnt lgkmcnt(0)
	v_mfma_f32_16x16x128_f8f6f4 v[126:129], v[140:147], v[172:179], v[126:129]
	v_mfma_f32_16x16x128_f8f6f4 v[118:121], v[148:155], v[172:179], v[118:121]
	v_mfma_f32_16x16x128_f8f6f4 v[110:113], v[140:147], v[180:187], v[110:113]
	v_mfma_f32_16x16x128_f8f6f4 v[102:105], v[148:155], v[180:187], v[102:105]
	v_mfma_f32_16x16x128_f8f6f4 v[204:207], v[140:147], v[188:195], v[92:95]
	v_mfma_f32_16x16x128_f8f6f4 v[208:211], v[148:155], v[188:195], v[84:87]
	v_mfma_f32_16x16x128_f8f6f4 v[212:215], v[140:147], v[196:203], v[76:79]
	v_mfma_f32_16x16x128_f8f6f4 v[218:221], v[148:155], v[196:203], v[68:71]
	s_setprio 0
	s_setprio 1
	v_mfma_f32_16x16x128_f8f6f4 v[122:125], v[156:163], v[172:179], v[122:125]
	v_mfma_f32_16x16x128_f8f6f4 v[114:117], v[164:171], v[172:179], v[114:117]
	v_mfma_f32_16x16x128_f8f6f4 v[106:109], v[156:163], v[180:187], v[106:109]
	v_mfma_f32_16x16x128_f8f6f4 v[98:101], v[164:171], v[180:187], v[98:101]
	v_mfma_f32_16x16x128_f8f6f4 v[172:175], v[156:163], v[188:195], v[88:91]
	v_mfma_f32_16x16x128_f8f6f4 v[176:179], v[164:171], v[188:195], v[80:83]
	v_mfma_f32_16x16x128_f8f6f4 v[180:183], v[156:163], v[196:203], v[72:75]
	v_mfma_f32_16x16x128_f8f6f4 v[184:187], v[164:171], v[196:203], v[64:67]
	s_setprio 0
	s_barrier
	v_mov_b32_e32 v96, v133
	s_add_i32 s42, s42, s23
	s_nop 2
	ds_read_b128 v[64:67], v139 offset:16384
	ds_read_b128 v[68:71], v139 offset:17408
	ds_read_b128 v[72:75], v139 offset:18432
	ds_read_b128 v[76:79], v139 offset:19456
	ds_read_b128 v[80:83], v139 offset:20480
	ds_read_b128 v[84:87], v139 offset:21504
	ds_read_b128 v[88:91], v139 offset:22528
	ds_read_b128 v[92:95], v139 offset:23552
	s_mov_b32 m0, s42
	s_nop 0
	global_load_lds_dwordx4 v96, s[20:21]
	v_mov_b32_e32 v96, v135
	s_add_i32 m0, s42, 0x2000
	s_add_u32 s42, s20, 0x40000
	global_load_lds_dwordx4 v96, s[20:21]
	s_addc_u32 s43, s21, 0
	v_mov_b32_e32 v96, v133
	s_add_i32 s46, s46, s23
	s_mov_b32 m0, s46
	s_nop 0
	global_load_lds_dwordx4 v96, s[42:43]
	v_mov_b32_e32 v96, v135
	s_add_i32 m0, s46, 0x2000
	s_nop 0
	global_load_lds_dwordx4 v96, s[42:43]
	v_mov_b32_e32 v96, v132
	s_mov_b32 m0, s24
	s_nop 0
	global_load_lds_dwordx4 v96, s[18:19]
	v_mov_b32_e32 v96, v134
	s_mov_b32 m0, s25
	s_nop 0
	global_load_lds_dwordx4 v96, s[18:19]
	s_waitcnt vmcnt(8)
	s_nop 0
	s_barrier
	s_setprio 1
	s_waitcnt lgkmcnt(0)
	v_mfma_f32_16x16x128_f8f6f4 v[60:63], v[140:147], v[64:71], v[60:63]
	v_mfma_f32_16x16x128_f8f6f4 v[52:55], v[148:155], v[64:71], v[52:55]
	v_mfma_f32_16x16x128_f8f6f4 v[44:47], v[140:147], v[72:79], v[44:47]
	v_mfma_f32_16x16x128_f8f6f4 v[196:199], v[148:155], v[72:79], v[36:39]
	v_mfma_f32_16x16x128_f8f6f4 v[200:203], v[140:147], v[80:87], v[28:31]
	v_mfma_f32_16x16x128_f8f6f4 v[222:225], v[148:155], v[80:87], v[20:23]
	v_mfma_f32_16x16x128_f8f6f4 v[226:229], v[140:147], v[88:95], v[12:15]
	v_mfma_f32_16x16x128_f8f6f4 v[230:233], v[148:155], v[88:95], v[4:7]
	s_setprio 0
	s_setprio 1
	v_mfma_f32_16x16x128_f8f6f4 v[56:59], v[156:163], v[64:71], v[56:59]
	v_mfma_f32_16x16x128_f8f6f4 v[48:51], v[164:171], v[64:71], v[48:51]
	v_mfma_f32_16x16x128_f8f6f4 v[40:43], v[156:163], v[72:79], v[40:43]
	v_mfma_f32_16x16x128_f8f6f4 v[234:237], v[164:171], v[72:79], v[32:35]
	v_mfma_f32_16x16x128_f8f6f4 v[238:241], v[156:163], v[80:87], v[24:27]
	v_mfma_f32_16x16x128_f8f6f4 v[242:245], v[164:171], v[80:87], v[16:19]
	v_mfma_f32_16x16x128_f8f6f4 v[246:249], v[156:163], v[88:95], v[8:11]
	v_mfma_f32_16x16x128_f8f6f4 v[250:253], v[164:171], v[88:95], v[0:3]
	s_setprio 0
	s_barrier
	s_add_i32 s46, 0, 0x18000
	s_nop 2
	v_add_u32_e32 v8, s46, v137
	s_add_i32 s47, 0, 0x1c000
	ds_read_b128 v[0:3], v8
	ds_read_b128 v[4:7], v8 offset:1024
	ds_read_b128 v[140:143], v8 offset:2048
	ds_read_b128 v[144:147], v8 offset:3072
	v_add_u32_e32 v8, s47, v137
	ds_read_b128 v[148:151], v8
	ds_read_b128 v[152:155], v8 offset:1024
	ds_read_b128 v[156:159], v8 offset:2048
	ds_read_b128 v[160:163], v8 offset:3072
	s_add_u32 s42, s18, 0x40000
	v_mov_b32_e32 v64, v132
	s_mov_b32 m0, s26
	ds_read_b128 v[8:11], v139 offset:32768
	ds_read_b128 v[12:15], v139 offset:33792
	ds_read_b128 v[16:19], v139 offset:34816
	ds_read_b128 v[20:23], v139 offset:35840
	ds_read_b128 v[24:27], v139 offset:36864
	ds_read_b128 v[28:31], v139 offset:37888
	ds_read_b128 v[32:35], v139 offset:38912
	ds_read_b128 v[36:39], v139 offset:39936
	s_addc_u32 s43, s19, 0
	s_nop 0
	global_load_lds_dwordx4 v64, s[42:43]
	v_mov_b32_e32 v64, v134
	s_mov_b32 m0, s27
	s_nop 0
	global_load_lds_dwordx4 v64, s[42:43]
	s_waitcnt vmcnt(8)
	s_nop 0
	s_barrier
	s_setprio 1
	s_waitcnt lgkmcnt(0)
	v_mfma_f32_16x16x128_f8f6f4 v[126:129], v[0:7], v[8:15], v[126:129]
	v_mfma_f32_16x16x128_f8f6f4 v[118:121], v[140:147], v[8:15], v[118:121]
	v_mfma_f32_16x16x128_f8f6f4 v[110:113], v[0:7], v[16:23], v[110:113]
	v_mfma_f32_16x16x128_f8f6f4 v[102:105], v[140:147], v[16:23], v[102:105]
	v_mfma_f32_16x16x128_f8f6f4 v[92:95], v[0:7], v[24:31], v[204:207]
	v_mfma_f32_16x16x128_f8f6f4 v[84:87], v[140:147], v[24:31], v[208:211]
	v_mfma_f32_16x16x128_f8f6f4 v[76:79], v[0:7], v[32:39], v[212:215]
	v_mfma_f32_16x16x128_f8f6f4 v[68:71], v[140:147], v[32:39], v[218:221]
	s_setprio 0
	s_setprio 1
	v_mfma_f32_16x16x128_f8f6f4 v[122:125], v[148:155], v[8:15], v[122:125]
	v_mfma_f32_16x16x128_f8f6f4 v[114:117], v[156:163], v[8:15], v[114:117]
	v_mfma_f32_16x16x128_f8f6f4 v[106:109], v[148:155], v[16:23], v[106:109]
	v_mfma_f32_16x16x128_f8f6f4 v[98:101], v[156:163], v[16:23], v[98:101]
	v_mfma_f32_16x16x128_f8f6f4 v[88:91], v[148:155], v[24:31], v[172:175]
	v_mfma_f32_16x16x128_f8f6f4 v[80:83], v[156:163], v[24:31], v[176:179]
	v_mfma_f32_16x16x128_f8f6f4 v[72:75], v[148:155], v[32:39], v[180:183]
	v_mfma_f32_16x16x128_f8f6f4 v[64:67], v[156:163], v[32:39], v[184:187]
	s_setprio 0
	s_barrier
	v_mov_b32_e32 v96, v133
	ds_read_b128 v[164:167], v139 offset:49152
	ds_read_b128 v[168:171], v139 offset:50176
	ds_read_b128 v[172:175], v139 offset:51200
	ds_read_b128 v[176:179], v139 offset:52224
	ds_read_b128 v[180:183], v139 offset:53248
	ds_read_b128 v[184:187], v139 offset:54272
	ds_read_b128 v[188:191], v139 offset:55296
	ds_read_b128 v[192:195], v139 offset:56320
	s_add_i32 s42, s46, s23
	v_lshl_add_u64 v[8:9], s[20:21], 0, v[96:97]
	v_lshl_add_u64 v[8:9], v[8:9], 0, s[0:1]
	s_mov_b32 m0, s42
	v_mov_b32_e32 v96, v135
	global_load_lds_dwordx4 v[8:9], off
	s_add_i32 m0, s42, 0x2000
	v_lshl_add_u64 v[8:9], s[20:21], 0, v[96:97]
	v_lshl_add_u64 v[8:9], v[8:9], 0, s[0:1]
	s_add_u32 s20, s20, 0x40080
	global_load_lds_dwordx4 v[8:9], off
	s_addc_u32 s21, s21, 0
	v_mov_b32_e32 v8, v133
	s_add_i32 s42, s47, s23
	s_mov_b32 m0, s42
	v_mov_b32_e32 v96, v132
	global_load_lds_dwordx4 v8, s[20:21]
	v_mov_b32_e32 v8, v135
	s_add_i32 m0, s42, 0x2000
	s_nop 0
	global_load_lds_dwordx4 v8, s[20:21]
	s_mov_b32 m0, s28
	v_lshl_add_u64 v[8:9], s[18:19], 0, v[96:97]
	v_lshl_add_u64 v[8:9], v[8:9], 0, s[0:1]
	v_mov_b32_e32 v96, v134
	global_load_lds_dwordx4 v[8:9], off
	s_mov_b32 m0, s29
	v_lshl_add_u64 v[8:9], s[18:19], 0, v[96:97]
	v_lshl_add_u64 v[8:9], v[8:9], 0, s[0:1]
	global_load_lds_dwordx4 v[8:9], off
	s_waitcnt vmcnt(8)
	s_nop 0
	s_barrier
	s_setprio 1
	s_waitcnt lgkmcnt(0)
	v_mfma_f32_16x16x128_f8f6f4 v[60:63], v[0:7], v[164:171], v[60:63]
	v_mfma_f32_16x16x128_f8f6f4 v[52:55], v[140:147], v[164:171], v[52:55]
	v_mfma_f32_16x16x128_f8f6f4 v[44:47], v[0:7], v[172:179], v[44:47]
	v_mfma_f32_16x16x128_f8f6f4 v[36:39], v[140:147], v[172:179], v[196:199]
	v_mfma_f32_16x16x128_f8f6f4 v[28:31], v[0:7], v[180:187], v[200:203]
	v_mfma_f32_16x16x128_f8f6f4 v[20:23], v[140:147], v[180:187], v[222:225]
	v_mfma_f32_16x16x128_f8f6f4 v[12:15], v[0:7], v[188:195], v[226:229]
	v_mfma_f32_16x16x128_f8f6f4 v[4:7], v[140:147], v[188:195], v[230:233]
	s_setprio 0
	s_setprio 1
	v_mfma_f32_16x16x128_f8f6f4 v[56:59], v[148:155], v[164:171], v[56:59]
	v_mfma_f32_16x16x128_f8f6f4 v[48:51], v[156:163], v[164:171], v[48:51]
	v_mfma_f32_16x16x128_f8f6f4 v[40:43], v[148:155], v[172:179], v[40:43]
	v_mfma_f32_16x16x128_f8f6f4 v[32:35], v[156:163], v[172:179], v[234:237]
	v_mfma_f32_16x16x128_f8f6f4 v[24:27], v[148:155], v[180:187], v[238:241]
	v_mfma_f32_16x16x128_f8f6f4 v[16:19], v[156:163], v[180:187], v[242:245]
	v_mfma_f32_16x16x128_f8f6f4 v[8:11], v[148:155], v[188:195], v[246:249]
	v_mfma_f32_16x16x128_f8f6f4 v[0:3], v[156:163], v[188:195], v[250:253]
	s_setprio 0
	s_barrier
	s_add_i32 s41, s41, 2
	s_add_u32 s39, s39, 0x100
	s_addc_u32 s40, s40, 0
	s_add_u32 s16, s16, 0x100
	s_addc_u32 s17, s17, 0
	s_cmp_gt_u32 s41, 13
	s_cbranch_scc0 .LBB0_2129
	s_and_b64 vcc, exec, s[6:7]
	s_cbranch_vccz .LBB0_2132
	s_barrier

.LBB0_2205:
	s_add_u32 s20, s18, 0xfff50080
	s_addc_u32 s21, s19, -1
	s_add_i32 s46, 0, 0x10000
	s_cmp_eq_u32 s43, 40
	s_cselect_b32 s21, s15, s21
	s_cselect_b32 s20, s14, s20
	v_add_u32_e32 v96, s46, v137
	s_cselect_b32 s23, s17, s42
	s_cselect_b32 s22, s16, s41
	s_add_i32 s69, 0, 0x14000
	ds_read_b128 v[140:143], v96
	ds_read_b128 v[144:147], v96 offset:1024
	ds_read_b128 v[148:151], v96 offset:2048
	ds_read_b128 v[152:155], v96 offset:3072
	v_add_u32_e32 v96, s69, v137
	ds_read_b128 v[156:159], v96
	ds_read_b128 v[160:163], v96 offset:1024
	ds_read_b128 v[164:167], v96 offset:2048
	ds_read_b128 v[168:171], v96 offset:3072
	v_mov_b32_e32 v96, v130
	ds_read_b128 v[172:175], v139
	ds_read_b128 v[176:179], v139 offset:1024
	ds_read_b128 v[180:183], v139 offset:2048
	ds_read_b128 v[184:187], v139 offset:3072
	ds_read_b128 v[188:191], v139 offset:4096
	ds_read_b128 v[192:195], v139 offset:5120
	ds_read_b128 v[196:199], v139 offset:6144
	ds_read_b128 v[200:203], v139 offset:7168
	s_add_i32 m0, s26, 0xc000
	s_nop 0
	global_load_lds_dwordx4 v96, s[18:19]
	v_mov_b32_e32 v96, v132
	s_add_i32 m0, s26, 0xe000
	s_nop 0
	global_load_lds_dwordx4 v96, s[18:19]
	s_waitcnt vmcnt(8)
	s_nop 0
	s_barrier
	s_setprio 1
	s_waitcnt lgkmcnt(0)
	v_mfma_f32_16x16x128_f8f6f4 v[126:129], v[140:147], v[172:179], v[126:129]
	v_mfma_f32_16x16x128_f8f6f4 v[122:125], v[148:155], v[172:179], v[122:125]
	v_mfma_f32_16x16x128_f8f6f4 v[118:121], v[140:147], v[180:187], v[118:121]
	v_mfma_f32_16x16x128_f8f6f4 v[110:113], v[148:155], v[180:187], v[110:113]
	v_mfma_f32_16x16x128_f8f6f4 v[102:105], v[140:147], v[188:195], v[102:105]
	v_mfma_f32_16x16x128_f8f6f4 v[204:207], v[148:155], v[188:195], v[92:95]
	v_mfma_f32_16x16x128_f8f6f4 v[208:211], v[140:147], v[196:203], v[84:87]
	v_mfma_f32_16x16x128_f8f6f4 v[212:215], v[148:155], v[196:203], v[76:79]
	s_setprio 0
	s_setprio 1
	v_mfma_f32_16x16x128_f8f6f4 v[114:117], v[156:163], v[172:179], v[114:117]
	v_mfma_f32_16x16x128_f8f6f4 v[106:109], v[164:171], v[172:179], v[106:109]
	v_mfma_f32_16x16x128_f8f6f4 v[98:101], v[156:163], v[180:187], v[98:101]
	v_mfma_f32_16x16x128_f8f6f4 v[172:175], v[164:171], v[180:187], v[88:91]
	v_mfma_f32_16x16x128_f8f6f4 v[176:179], v[156:163], v[188:195], v[80:83]
	v_mfma_f32_16x16x128_f8f6f4 v[180:183], v[164:171], v[188:195], v[72:75]
	v_mfma_f32_16x16x128_f8f6f4 v[184:187], v[156:163], v[196:203], v[68:71]
	v_mfma_f32_16x16x128_f8f6f4 v[188:191], v[164:171], v[196:203], v[64:67]
	s_setprio 0
	s_barrier
	v_mov_b32_e32 v96, v131
	s_add_i32 s46, s46, s25
	s_nop 2
	ds_read_b128 v[64:67], v139 offset:16384
	ds_read_b128 v[68:71], v139 offset:17408
	ds_read_b128 v[72:75], v139 offset:18432
	ds_read_b128 v[76:79], v139 offset:19456
	ds_read_b128 v[80:83], v139 offset:20480
	ds_read_b128 v[84:87], v139 offset:21504
	ds_read_b128 v[88:91], v139 offset:22528
	ds_read_b128 v[92:95], v139 offset:23552
	s_mov_b32 m0, s46
	s_nop 0
	global_load_lds_dwordx4 v96, s[22:23]
	v_mov_b32_e32 v96, v133
	s_add_i32 m0, s46, 0x2000
	s_add_u32 s46, s22, 0xb0000
	global_load_lds_dwordx4 v96, s[22:23]
	s_addc_u32 s47, s23, 0
	v_mov_b32_e32 v96, v131
	s_add_i32 s69, s69, s25
	s_mov_b32 m0, s69
	s_nop 0
	global_load_lds_dwordx4 v96, s[46:47]
	v_mov_b32_e32 v96, v133
	s_add_i32 m0, s69, 0x2000
	s_nop 0
	global_load_lds_dwordx4 v96, s[46:47]
	v_mov_b32_e32 v96, v130
	s_mov_b32 m0, s26
	s_nop 0
	global_load_lds_dwordx4 v96, s[20:21]
	v_mov_b32_e32 v96, v132
	s_mov_b32 m0, s27
	s_nop 0
	global_load_lds_dwordx4 v96, s[20:21]
	s_waitcnt vmcnt(8)
	s_nop 0
	s_barrier
	s_setprio 1
	s_waitcnt lgkmcnt(0)
	v_mfma_f32_16x16x128_f8f6f4 v[60:63], v[140:147], v[64:71], v[60:63]
	v_mfma_f32_16x16x128_f8f6f4 v[56:59], v[148:155], v[64:71], v[56:59]
	v_mfma_f32_16x16x128_f8f6f4 v[52:55], v[140:147], v[72:79], v[52:55]
	v_mfma_f32_16x16x128_f8f6f4 v[192:195], v[148:155], v[72:79], v[44:47]
	v_mfma_f32_16x16x128_f8f6f4 v[196:199], v[140:147], v[80:87], v[36:39]
	v_mfma_f32_16x16x128_f8f6f4 v[200:203], v[148:155], v[80:87], v[28:31]
	v_mfma_f32_16x16x128_f8f6f4 v[218:221], v[140:147], v[88:95], v[20:23]
	v_mfma_f32_16x16x128_f8f6f4 v[222:225], v[148:155], v[88:95], v[12:15]
	s_setprio 0
	s_setprio 1
	v_mfma_f32_16x16x128_f8f6f4 v[48:51], v[156:163], v[64:71], v[48:51]
	v_mfma_f32_16x16x128_f8f6f4 v[226:229], v[164:171], v[64:71], v[40:43]
	v_mfma_f32_16x16x128_f8f6f4 v[230:233], v[156:163], v[72:79], v[32:35]
	v_mfma_f32_16x16x128_f8f6f4 v[234:237], v[164:171], v[72:79], v[24:27]
	v_mfma_f32_16x16x128_f8f6f4 v[238:241], v[156:163], v[80:87], v[16:19]
	v_mfma_f32_16x16x128_f8f6f4 v[242:245], v[164:171], v[80:87], v[8:11]
	v_mfma_f32_16x16x128_f8f6f4 v[246:249], v[156:163], v[88:95], v[4:7]
	v_mfma_f32_16x16x128_f8f6f4 v[250:253], v[164:171], v[88:95], v[0:3]
	s_setprio 0
	s_barrier
	s_add_i32 s69, 0, 0x18000
	s_add_i32 s76, 0, 0x1c000
	v_add_u32_e32 v12, s69, v137
	v_add_u32_e32 v16, s76, v137
	s_nop 0
	ds_read_b128 v[0:3], v12
	ds_read_b128 v[4:7], v12 offset:1024
	ds_read_b128 v[8:11], v12 offset:2048
	ds_read_b128 v[12:15], v12 offset:3072
	ds_read_b128 v[140:143], v16
	ds_read_b128 v[144:147], v16 offset:1024
	ds_read_b128 v[148:151], v16 offset:2048
	ds_read_b128 v[152:155], v16 offset:3072
	s_add_u32 s46, s20, 0xb0000
	v_mov_b32_e32 v64, v130
	s_mov_b32 m0, s28
	ds_read_b128 v[16:19], v139 offset:32768
	ds_read_b128 v[20:23], v139 offset:33792
	ds_read_b128 v[24:27], v139 offset:34816
	ds_read_b128 v[28:31], v139 offset:35840
	ds_read_b128 v[32:35], v139 offset:36864
	ds_read_b128 v[36:39], v139 offset:37888
	ds_read_b128 v[40:43], v139 offset:38912
	ds_read_b128 v[44:47], v139 offset:39936
	s_addc_u32 s47, s21, 0
	s_nop 0
	global_load_lds_dwordx4 v64, s[46:47]
	v_mov_b32_e32 v64, v132
	s_mov_b32 m0, s29
	s_nop 0
	global_load_lds_dwordx4 v64, s[46:47]
	s_waitcnt vmcnt(8)
	s_nop 0
	s_barrier
	s_setprio 1
	s_waitcnt lgkmcnt(0)
	v_mfma_f32_16x16x128_f8f6f4 v[126:129], v[0:7], v[16:23], v[126:129]
	v_mfma_f32_16x16x128_f8f6f4 v[122:125], v[8:15], v[16:23], v[122:125]
	v_mfma_f32_16x16x128_f8f6f4 v[118:121], v[0:7], v[24:31], v[118:121]
	v_mfma_f32_16x16x128_f8f6f4 v[110:113], v[8:15], v[24:31], v[110:113]
	v_mfma_f32_16x16x128_f8f6f4 v[102:105], v[0:7], v[32:39], v[102:105]
	v_mfma_f32_16x16x128_f8f6f4 v[92:95], v[8:15], v[32:39], v[204:207]
	v_mfma_f32_16x16x128_f8f6f4 v[84:87], v[0:7], v[40:47], v[208:211]
	v_mfma_f32_16x16x128_f8f6f4 v[76:79], v[8:15], v[40:47], v[212:215]
	s_setprio 0
	s_setprio 1
	v_mfma_f32_16x16x128_f8f6f4 v[114:117], v[140:147], v[16:23], v[114:117]
	v_mfma_f32_16x16x128_f8f6f4 v[106:109], v[148:155], v[16:23], v[106:109]
	v_mfma_f32_16x16x128_f8f6f4 v[98:101], v[140:147], v[24:31], v[98:101]
	v_mfma_f32_16x16x128_f8f6f4 v[88:91], v[148:155], v[24:31], v[172:175]
	v_mfma_f32_16x16x128_f8f6f4 v[80:83], v[140:147], v[32:39], v[176:179]
	v_mfma_f32_16x16x128_f8f6f4 v[72:75], v[148:155], v[32:39], v[180:183]
	v_mfma_f32_16x16x128_f8f6f4 v[68:71], v[140:147], v[40:47], v[184:187]
	v_mfma_f32_16x16x128_f8f6f4 v[64:67], v[148:155], v[40:47], v[188:191]
	s_setprio 0
	s_barrier
	v_mov_b32_e32 v96, v131
	ds_read_b128 v[156:159], v139 offset:49152
	ds_read_b128 v[160:163], v139 offset:50176
	ds_read_b128 v[164:167], v139 offset:51200
	ds_read_b128 v[168:171], v139 offset:52224
	ds_read_b128 v[172:175], v139 offset:53248
	ds_read_b128 v[176:179], v139 offset:54272
	ds_read_b128 v[180:183], v139 offset:55296
	ds_read_b128 v[184:187], v139 offset:56320
	s_add_i32 s46, s69, s25
	v_lshl_add_u64 v[16:17], s[22:23], 0, v[96:97]
	v_lshl_add_u64 v[16:17], v[16:17], 0, s[0:1]
	s_mov_b32 m0, s46
	v_mov_b32_e32 v96, v133
	global_load_lds_dwordx4 v[16:17], off
	s_add_i32 m0, s46, 0x2000
	v_lshl_add_u64 v[16:17], s[22:23], 0, v[96:97]
	v_lshl_add_u64 v[16:17], v[16:17], 0, s[0:1]
	s_add_u32 s22, s22, 0xb0080
	global_load_lds_dwordx4 v[16:17], off
	s_addc_u32 s23, s23, 0
	v_mov_b32_e32 v16, v131
	s_add_i32 s46, s76, s25
	s_mov_b32 m0, s46
	v_mov_b32_e32 v96, v130
	global_load_lds_dwordx4 v16, s[22:23]
	v_mov_b32_e32 v16, v133
	s_add_i32 m0, s46, 0x2000
	s_nop 0
	global_load_lds_dwordx4 v16, s[22:23]
	s_mov_b32 m0, s30
	v_lshl_add_u64 v[16:17], s[20:21], 0, v[96:97]
	v_lshl_add_u64 v[16:17], v[16:17], 0, s[0:1]
	v_mov_b32_e32 v96, v132
	global_load_lds_dwordx4 v[16:17], off
	s_mov_b32 m0, s31
	v_lshl_add_u64 v[16:17], s[20:21], 0, v[96:97]
	v_lshl_add_u64 v[16:17], v[16:17], 0, s[0:1]
	global_load_lds_dwordx4 v[16:17], off
	s_waitcnt vmcnt(8)
	s_nop 0
	s_barrier
	s_setprio 1
	s_waitcnt lgkmcnt(0)
	v_mfma_f32_16x16x128_f8f6f4 v[60:63], v[0:7], v[156:163], v[60:63]
	v_mfma_f32_16x16x128_f8f6f4 v[56:59], v[8:15], v[156:163], v[56:59]
	v_mfma_f32_16x16x128_f8f6f4 v[52:55], v[0:7], v[164:171], v[52:55]
	v_mfma_f32_16x16x128_f8f6f4 v[44:47], v[8:15], v[164:171], v[192:195]
	v_mfma_f32_16x16x128_f8f6f4 v[36:39], v[0:7], v[172:179], v[196:199]
	v_mfma_f32_16x16x128_f8f6f4 v[28:31], v[8:15], v[172:179], v[200:203]
	v_mfma_f32_16x16x128_f8f6f4 v[20:23], v[0:7], v[180:187], v[218:221]
	v_mfma_f32_16x16x128_f8f6f4 v[12:15], v[8:15], v[180:187], v[222:225]
	s_setprio 0
	s_setprio 1
	v_mfma_f32_16x16x128_f8f6f4 v[48:51], v[140:147], v[156:163], v[48:51]
	v_mfma_f32_16x16x128_f8f6f4 v[40:43], v[148:155], v[156:163], v[226:229]
	v_mfma_f32_16x16x128_f8f6f4 v[32:35], v[140:147], v[164:171], v[230:233]
	v_mfma_f32_16x16x128_f8f6f4 v[24:27], v[148:155], v[164:171], v[234:237]
	v_mfma_f32_16x16x128_f8f6f4 v[16:19], v[140:147], v[172:179], v[238:241]
	v_mfma_f32_16x16x128_f8f6f4 v[8:11], v[148:155], v[172:179], v[242:245]
	v_mfma_f32_16x16x128_f8f6f4 v[4:7], v[140:147], v[180:187], v[246:249]
	v_mfma_f32_16x16x128_f8f6f4 v[0:3], v[148:155], v[180:187], v[250:253]
	s_setprio 0
	s_barrier
	s_add_i32 s43, s43, 2
	s_add_u32 s41, s41, 0x100
	s_addc_u32 s42, s42, 0
	s_add_u32 s18, s18, 0x100
	s_addc_u32 s19, s19, 0
	s_cmp_gt_u32 s43, 41
	s_cbranch_scc0 .LBB0_2205
	s_and_b64 vcc, exec, s[8:9]
	s_cbranch_vccz .LBB0_2208
	s_barrier

.LBB0_2227:
	s_add_i32 s83, s20, 2
	s_add_u32 s22, s18, 0xfff50080
	s_addc_u32 s21, s19, -1
	s_add_i32 s84, 0, 0x10000
	s_cmp_eq_u32 s80, s20
	s_cselect_b32 s21, s15, s21
	s_cselect_b32 s20, s14, s22
	v_add_u32_e32 v96, s84, v145
	s_cselect_b32 s23, s17, s82
	s_cselect_b32 s22, s16, s81
	s_add_i32 s86, 0, 0x14000
	ds_read_b128 v[148:151], v96
	ds_read_b128 v[152:155], v96 offset:1024
	ds_read_b128 v[156:159], v96 offset:2048
	ds_read_b128 v[160:163], v96 offset:3072
	v_add_u32_e32 v96, s86, v145
	ds_read_b128 v[164:167], v96
	ds_read_b128 v[168:171], v96 offset:1024
	ds_read_b128 v[172:175], v96 offset:2048
	ds_read_b128 v[176:179], v96 offset:3072
	v_mov_b32_e32 v96, v138
	ds_read_b128 v[180:183], v147
	ds_read_b128 v[184:187], v147 offset:1024
	ds_read_b128 v[188:191], v147 offset:2048
	ds_read_b128 v[192:195], v147 offset:3072
	ds_read_b128 v[196:199], v147 offset:4096
	ds_read_b128 v[200:203], v147 offset:5120
	ds_read_b128 v[222:225], v147 offset:6144
	ds_read_b128 v[226:229], v147 offset:7168
	s_add_i32 m0, s26, 0xc000
	s_nop 0
	global_load_lds_dwordx4 v96, s[18:19]
	v_mov_b32_e32 v96, v140
	s_add_i32 m0, s26, 0xe000
	s_nop 0
	global_load_lds_dwordx4 v96, s[18:19]
	s_waitcnt vmcnt(8)
	s_nop 0
	s_barrier
	s_setprio 1
	s_waitcnt lgkmcnt(0)
	v_mfma_f32_16x16x128_f8f6f4 v[126:129], v[148:155], v[188:195], v[126:129]
	v_mfma_f32_16x16x128_f8f6f4 v[110:113], v[156:163], v[188:195], v[110:113]
	v_mfma_f32_16x16x128_f8f6f4 v[130:133], v[148:155], v[196:203], v[130:133]
	v_mfma_f32_16x16x128_f8f6f4 v[114:117], v[156:163], v[196:203], v[114:117]
	v_mfma_f32_16x16x128_f8f6f4 v[134:137], v[148:155], v[222:229], v[134:137]
	v_mfma_f32_16x16x128_f8f6f4 v[118:121], v[156:163], v[222:229], v[118:121]
	v_mfma_f32_16x16x128_f8f6f4 v[106:109], v[148:155], v[180:187], v[64:67]
	v_mfma_f32_16x16x128_f8f6f4 v[122:125], v[156:163], v[180:187], v[88:91]
	s_setprio 0
	s_setprio 1
	v_mfma_f32_16x16x128_f8f6f4 v[92:95], v[164:171], v[180:187], v[92:95]
	v_mfma_f32_16x16x128_f8f6f4 v[68:71], v[172:179], v[180:187], v[68:71]
	v_mfma_f32_16x16x128_f8f6f4 v[180:183], v[164:171], v[188:195], v[98:101]
	v_mfma_f32_16x16x128_f8f6f4 v[184:187], v[172:179], v[188:195], v[80:83]
	v_mfma_f32_16x16x128_f8f6f4 v[188:191], v[164:171], v[196:203], v[102:105]
	v_mfma_f32_16x16x128_f8f6f4 v[192:195], v[172:179], v[196:203], v[84:87]
	v_mfma_f32_16x16x128_f8f6f4 v[196:199], v[164:171], v[222:229], v[76:79]
	v_mfma_f32_16x16x128_f8f6f4 v[200:203], v[172:179], v[222:229], v[60:63]
	s_setprio 0
	s_barrier
	v_mov_b32_e32 v96, v139
	s_add_i32 s84, s84, s25
	s_nop 2
	ds_read_b128 v[60:63], v147 offset:16384
	ds_read_b128 v[64:67], v147 offset:17408
	ds_read_b128 v[76:79], v147 offset:18432
	ds_read_b128 v[80:83], v147 offset:19456
	ds_read_b128 v[84:87], v147 offset:20480
	ds_read_b128 v[88:91], v147 offset:21504
	ds_read_b128 v[98:101], v147 offset:22528
	ds_read_b128 v[102:105], v147 offset:23552
	s_mov_b32 m0, s84
	s_nop 0
	global_load_lds_dwordx4 v96, s[22:23]
	v_mov_b32_e32 v96, v141
	s_add_i32 m0, s84, 0x2000
	s_add_u32 s84, s22, 0xb0000
	global_load_lds_dwordx4 v96, s[22:23]
	s_addc_u32 s85, s23, 0
	v_mov_b32_e32 v96, v139
	s_add_i32 s86, s86, s25
	s_mov_b32 m0, s86
	s_nop 0
	global_load_lds_dwordx4 v96, s[84:85]
	v_mov_b32_e32 v96, v141
	s_add_i32 m0, s86, 0x2000
	s_nop 0
	global_load_lds_dwordx4 v96, s[84:85]
	v_mov_b32_e32 v96, v138
	s_mov_b32 m0, s26
	s_nop 0
	global_load_lds_dwordx4 v96, s[20:21]
	v_mov_b32_e32 v96, v140
	s_mov_b32 m0, s27
	s_nop 0
	global_load_lds_dwordx4 v96, s[20:21]
	s_waitcnt vmcnt(8)
	s_nop 0
	s_barrier
	s_setprio 1
	s_waitcnt lgkmcnt(0)
	v_mfma_f32_16x16x128_f8f6f4 v[72:75], v[148:155], v[60:67], v[72:75]
	v_mfma_f32_16x16x128_f8f6f4 v[56:59], v[156:163], v[60:67], v[56:59]
	v_mfma_f32_16x16x128_f8f6f4 v[52:55], v[148:155], v[76:83], v[52:55]
	v_mfma_f32_16x16x128_f8f6f4 v[48:51], v[156:163], v[76:83], v[48:51]
	v_mfma_f32_16x16x128_f8f6f4 v[204:207], v[148:155], v[84:91], v[40:43]
	v_mfma_f32_16x16x128_f8f6f4 v[208:211], v[156:163], v[84:91], v[32:35]
	v_mfma_f32_16x16x128_f8f6f4 v[212:215], v[148:155], v[98:105], v[24:27]
	v_mfma_f32_16x16x128_f8f6f4 v[218:221], v[156:163], v[98:105], v[16:19]
	s_setprio 0
	s_setprio 1
	v_mfma_f32_16x16x128_f8f6f4 v[222:225], v[164:171], v[60:67], v[44:47]
	v_mfma_f32_16x16x128_f8f6f4 v[226:229], v[172:179], v[60:67], v[36:39]
	v_mfma_f32_16x16x128_f8f6f4 v[230:233], v[164:171], v[76:83], v[28:31]
	v_mfma_f32_16x16x128_f8f6f4 v[234:237], v[172:179], v[76:83], v[20:23]
	v_mfma_f32_16x16x128_f8f6f4 v[238:241], v[164:171], v[84:91], v[12:15]
	v_mfma_f32_16x16x128_f8f6f4 v[242:245], v[172:179], v[84:91], v[8:11]
	v_mfma_f32_16x16x128_f8f6f4 v[246:249], v[164:171], v[98:105], v[4:7]
	v_mfma_f32_16x16x128_f8f6f4 v[250:253], v[172:179], v[98:105], v[0:3]
	s_setprio 0
	s_barrier
	s_add_i32 s86, 0, 0x18000
	s_add_i32 s87, 0, 0x1c000
	v_add_u32_e32 v12, s86, v145
	v_add_u32_e32 v16, s87, v145
	s_nop 0
	ds_read_b128 v[0:3], v12
	ds_read_b128 v[4:7], v12 offset:1024
	ds_read_b128 v[8:11], v12 offset:2048
	ds_read_b128 v[12:15], v12 offset:3072
	ds_read_b128 v[148:151], v16
	ds_read_b128 v[152:155], v16 offset:1024
	ds_read_b128 v[156:159], v16 offset:2048
	ds_read_b128 v[160:163], v16 offset:3072
	s_add_u32 s84, s20, 0xb0000
	v_mov_b32_e32 v60, v138
	s_mov_b32 m0, s28
	ds_read_b128 v[16:19], v147 offset:32768
	ds_read_b128 v[20:23], v147 offset:33792
	ds_read_b128 v[24:27], v147 offset:34816
	ds_read_b128 v[28:31], v147 offset:35840
	ds_read_b128 v[32:35], v147 offset:36864
	ds_read_b128 v[36:39], v147 offset:37888
	ds_read_b128 v[40:43], v147 offset:38912
	ds_read_b128 v[44:47], v147 offset:39936
	s_addc_u32 s85, s21, 0
	s_nop 0
	global_load_lds_dwordx4 v60, s[84:85]
	v_mov_b32_e32 v60, v140
	s_mov_b32 m0, s29
	s_nop 0
	global_load_lds_dwordx4 v60, s[84:85]
	s_waitcnt vmcnt(8)
	s_nop 0
	s_barrier
	s_setprio 1
	s_waitcnt lgkmcnt(0)
	v_mfma_f32_16x16x128_f8f6f4 v[64:67], v[0:7], v[16:23], v[106:109]
	v_mfma_f32_16x16x128_f8f6f4 v[88:91], v[8:15], v[16:23], v[122:125]
	v_mfma_f32_16x16x128_f8f6f4 v[126:129], v[0:7], v[24:31], v[126:129]
	v_mfma_f32_16x16x128_f8f6f4 v[110:113], v[8:15], v[24:31], v[110:113]
	v_mfma_f32_16x16x128_f8f6f4 v[130:133], v[0:7], v[32:39], v[130:133]
	v_mfma_f32_16x16x128_f8f6f4 v[114:117], v[8:15], v[32:39], v[114:117]
	v_mfma_f32_16x16x128_f8f6f4 v[134:137], v[0:7], v[40:47], v[134:137]
	v_mfma_f32_16x16x128_f8f6f4 v[118:121], v[8:15], v[40:47], v[118:121]
	s_setprio 0
	s_setprio 1
	v_mfma_f32_16x16x128_f8f6f4 v[92:95], v[148:155], v[16:23], v[92:95]
	v_mfma_f32_16x16x128_f8f6f4 v[68:71], v[156:163], v[16:23], v[68:71]
	v_mfma_f32_16x16x128_f8f6f4 v[98:101], v[148:155], v[24:31], v[180:183]
	v_mfma_f32_16x16x128_f8f6f4 v[80:83], v[156:163], v[24:31], v[184:187]
	v_mfma_f32_16x16x128_f8f6f4 v[102:105], v[148:155], v[32:39], v[188:191]
	v_mfma_f32_16x16x128_f8f6f4 v[84:87], v[156:163], v[32:39], v[192:195]
	v_mfma_f32_16x16x128_f8f6f4 v[76:79], v[148:155], v[40:47], v[196:199]
	v_mfma_f32_16x16x128_f8f6f4 v[60:63], v[156:163], v[40:47], v[200:203]
	s_setprio 0
	s_barrier
	v_mov_b32_e32 v96, v139
	ds_read_b128 v[164:167], v147 offset:49152
	ds_read_b128 v[168:171], v147 offset:50176
	ds_read_b128 v[172:175], v147 offset:51200
	ds_read_b128 v[176:179], v147 offset:52224
	ds_read_b128 v[180:183], v147 offset:53248
	ds_read_b128 v[184:187], v147 offset:54272
	ds_read_b128 v[188:191], v147 offset:55296
	ds_read_b128 v[192:195], v147 offset:56320
	s_add_i32 s84, s86, s25
	v_lshl_add_u64 v[16:17], s[22:23], 0, v[96:97]
	v_lshl_add_u64 v[16:17], v[16:17], 0, s[0:1]
	s_mov_b32 m0, s84
	v_mov_b32_e32 v96, v141
	global_load_lds_dwordx4 v[16:17], off
	s_add_i32 m0, s84, 0x2000
	v_lshl_add_u64 v[16:17], s[22:23], 0, v[96:97]
	v_lshl_add_u64 v[16:17], v[16:17], 0, s[0:1]
	s_add_u32 s22, s22, 0xb0080
	global_load_lds_dwordx4 v[16:17], off
	s_addc_u32 s23, s23, 0
	v_mov_b32_e32 v16, v139
	s_add_i32 s84, s87, s25
	s_mov_b32 m0, s84
	v_mov_b32_e32 v96, v138
	global_load_lds_dwordx4 v16, s[22:23]
	v_mov_b32_e32 v16, v141
	s_add_i32 m0, s84, 0x2000
	s_nop 0
	global_load_lds_dwordx4 v16, s[22:23]
	s_mov_b32 m0, s35
	v_lshl_add_u64 v[16:17], s[20:21], 0, v[96:97]
	v_lshl_add_u64 v[16:17], v[16:17], 0, s[0:1]
	v_mov_b32_e32 v96, v140
	global_load_lds_dwordx4 v[16:17], off
	s_mov_b32 m0, s36
	v_lshl_add_u64 v[16:17], s[20:21], 0, v[96:97]
	v_lshl_add_u64 v[16:17], v[16:17], 0, s[0:1]
	global_load_lds_dwordx4 v[16:17], off
	s_waitcnt vmcnt(8)
	s_nop 0
	s_barrier
	s_setprio 1
	s_waitcnt lgkmcnt(0)
	v_mfma_f32_16x16x128_f8f6f4 v[72:75], v[0:7], v[164:171], v[72:75]
	v_mfma_f32_16x16x128_f8f6f4 v[56:59], v[8:15], v[164:171], v[56:59]
	v_mfma_f32_16x16x128_f8f6f4 v[52:55], v[0:7], v[172:179], v[52:55]
	v_mfma_f32_16x16x128_f8f6f4 v[48:51], v[8:15], v[172:179], v[48:51]
	v_mfma_f32_16x16x128_f8f6f4 v[40:43], v[0:7], v[180:187], v[204:207]
	v_mfma_f32_16x16x128_f8f6f4 v[32:35], v[8:15], v[180:187], v[208:211]
	v_mfma_f32_16x16x128_f8f6f4 v[24:27], v[0:7], v[188:195], v[212:215]
	v_mfma_f32_16x16x128_f8f6f4 v[16:19], v[8:15], v[188:195], v[218:221]
	s_setprio 0
	s_setprio 1
	v_mfma_f32_16x16x128_f8f6f4 v[44:47], v[148:155], v[164:171], v[222:225]
	v_mfma_f32_16x16x128_f8f6f4 v[36:39], v[156:163], v[164:171], v[226:229]
	v_mfma_f32_16x16x128_f8f6f4 v[28:31], v[148:155], v[172:179], v[230:233]
	v_mfma_f32_16x16x128_f8f6f4 v[20:23], v[156:163], v[172:179], v[234:237]
	v_mfma_f32_16x16x128_f8f6f4 v[12:15], v[148:155], v[180:187], v[238:241]
	v_mfma_f32_16x16x128_f8f6f4 v[8:11], v[156:163], v[180:187], v[242:245]
	v_mfma_f32_16x16x128_f8f6f4 v[4:7], v[148:155], v[188:195], v[246:249]
	v_mfma_f32_16x16x128_f8f6f4 v[0:3], v[156:163], v[188:195], v[250:253]
	s_setprio 0
	s_barrier
	s_add_u32 s81, s81, 0x100
	s_addc_u32 s82, s82, 0
	s_add_u32 s18, s18, 0x100
	s_addc_u32 s19, s19, 0
	s_cmp_ge_i32 s83, s79
	s_mov_b32 s20, s83
	s_cbranch_scc0 .LBB0_2227
	v_pk_mul_f32 v[66:67], v[66:67], s[58:59] op_sel_hi:[1,0]
	v_pk_mul_f32 v[64:65], v[64:65], s[58:59] op_sel_hi:[1,0]
	v_pk_mul_f32 v[90:91], v[90:91], s[58:59] op_sel_hi:[1,0]
	v_pk_mul_f32 v[88:89], v[88:89], s[58:59] op_sel_hi:[1,0]
	v_pk_mul_f32 v[108:109], v[94:95], s[58:59] op_sel_hi:[1,0]
	v_pk_mul_f32 v[106:107], v[92:93], s[58:59] op_sel_hi:[1,0]
	v_pk_mul_f32 v[124:125], v[70:71], s[58:59] op_sel_hi:[1,0]
	v_pk_mul_f32 v[122:123], v[68:69], s[58:59] op_sel_hi:[1,0]
	v_pk_mul_f32 v[70:71], v[128:129], s[58:59] op_sel_hi:[1,0]
	v_pk_mul_f32 v[68:69], v[126:127], s[58:59] op_sel_hi:[1,0]
	v_pk_mul_f32 v[94:95], v[112:113], s[58:59] op_sel_hi:[1,0]
	v_pk_mul_f32 v[92:93], v[110:111], s[58:59] op_sel_hi:[1,0]
	v_pk_mul_f32 v[112:113], v[100:101], s[58:59] op_sel_hi:[1,0]
	v_pk_mul_f32 v[110:111], v[98:99], s[58:59] op_sel_hi:[1,0]
	v_pk_mul_f32 v[128:129], v[82:83], s[58:59] op_sel_hi:[1,0]
	v_pk_mul_f32 v[126:127], v[80:81], s[58:59] op_sel_hi:[1,0]
	v_pk_mul_f32 v[82:83], v[132:133], s[58:59] op_sel_hi:[1,0]
	v_pk_mul_f32 v[80:81], v[130:131], s[58:59] op_sel_hi:[1,0]
	v_pk_mul_f32 v[100:101], v[116:117], s[58:59] op_sel_hi:[1,0]
	v_pk_mul_f32 v[98:99], v[114:115], s[58:59] op_sel_hi:[1,0]
	v_pk_mul_f32 v[116:117], v[104:105], s[58:59] op_sel_hi:[1,0]
	v_pk_mul_f32 v[114:115], v[102:103], s[58:59] op_sel_hi:[1,0]
	v_pk_mul_f32 v[132:133], v[86:87], s[58:59] op_sel_hi:[1,0]
	v_pk_mul_f32 v[130:131], v[84:85], s[58:59] op_sel_hi:[1,0]
	v_pk_mul_f32 v[86:87], v[136:137], s[58:59] op_sel_hi:[1,0]
	v_pk_mul_f32 v[84:85], v[134:135], s[58:59] op_sel_hi:[1,0]
	v_pk_mul_f32 v[104:105], v[120:121], s[58:59] op_sel_hi:[1,0]
	v_pk_mul_f32 v[102:103], v[118:119], s[58:59] op_sel_hi:[1,0]
	v_pk_mul_f32 v[78:79], v[78:79], s[58:59] op_sel_hi:[1,0]
	v_pk_mul_f32 v[76:77], v[76:77], s[58:59] op_sel_hi:[1,0]
	v_pk_mul_f32 v[120:121], v[62:63], s[58:59] op_sel_hi:[1,0]
	v_pk_mul_f32 v[118:119], v[60:61], s[58:59] op_sel_hi:[1,0]
	v_pk_mul_f32 v[62:63], v[74:75], s[58:59] op_sel_hi:[1,0]
	v_pk_mul_f32 v[60:61], v[72:73], s[58:59] op_sel_hi:[1,0]
	v_pk_mul_f32 v[58:59], v[58:59], s[58:59] op_sel_hi:[1,0]
	v_pk_mul_f32 v[56:57], v[56:57], s[58:59] op_sel_hi:[1,0]
	v_pk_mul_f32 v[74:75], v[46:47], s[58:59] op_sel_hi:[1,0]
	v_pk_mul_f32 v[72:73], v[44:45], s[58:59] op_sel_hi:[1,0]
	v_pk_mul_f32 v[136:137], v[38:39], s[58:59] op_sel_hi:[1,0]
	v_pk_mul_f32 v[134:135], v[36:37], s[58:59] op_sel_hi:[1,0]
	v_pk_mul_f32 v[38:39], v[54:55], s[58:59] op_sel_hi:[1,0]
	v_pk_mul_f32 v[36:37], v[52:53], s[58:59] op_sel_hi:[1,0]
	v_pk_mul_f32 v[46:47], v[50:51], s[58:59] op_sel_hi:[1,0]
	v_pk_mul_f32 v[44:45], v[48:49], s[58:59] op_sel_hi:[1,0]
	v_pk_mul_f32 v[50:51], v[30:31], s[58:59] op_sel_hi:[1,0]
	v_pk_mul_f32 v[48:49], v[28:29], s[58:59] op_sel_hi:[1,0]
	v_pk_mul_f32 v[54:55], v[22:23], s[58:59] op_sel_hi:[1,0]
	v_pk_mul_f32 v[52:53], v[20:21], s[58:59] op_sel_hi:[1,0]
	v_pk_mul_f32 v[22:23], v[42:43], s[58:59] op_sel_hi:[1,0]
	v_pk_mul_f32 v[20:21], v[40:41], s[58:59] op_sel_hi:[1,0]
	v_pk_mul_f32 v[30:31], v[34:35], s[58:59] op_sel_hi:[1,0]
	v_pk_mul_f32 v[28:29], v[32:33], s[58:59] op_sel_hi:[1,0]
	v_pk_mul_f32 v[34:35], v[14:15], s[58:59] op_sel_hi:[1,0]
	v_pk_mul_f32 v[32:33], v[12:13], s[58:59] op_sel_hi:[1,0]
	v_pk_mul_f32 v[42:43], v[10:11], s[58:59] op_sel_hi:[1,0]
	v_pk_mul_f32 v[40:41], v[8:9], s[58:59] op_sel_hi:[1,0]
	v_pk_mul_f32 v[10:11], v[26:27], s[58:59] op_sel_hi:[1,0]
	v_pk_mul_f32 v[8:9], v[24:25], s[58:59] op_sel_hi:[1,0]
	v_pk_mul_f32 v[14:15], v[18:19], s[58:59] op_sel_hi:[1,0]
	v_pk_mul_f32 v[12:13], v[16:17], s[58:59] op_sel_hi:[1,0]
	v_pk_mul_f32 v[6:7], v[6:7], s[58:59] op_sel_hi:[1,0]
	v_pk_mul_f32 v[4:5], v[4:5], s[58:59] op_sel_hi:[1,0]
	v_pk_mul_f32 v[2:3], v[2:3], s[58:59] op_sel_hi:[1,0]
	v_pk_mul_f32 v[0:1], v[0:1], s[58:59] op_sel_hi:[1,0]
	s_and_b64 vcc, exec, s[8:9]
	s_cbranch_vccz .LBB0_2230
